# baseline (speedup 1.0000x reference)
.Lrs_a_4:
	s_add_u32 s81, s40, s22
	s_addc_u32 s82, s41, s23
	s_add_u32 s29, s40, 0x100
	s_addc_u32 s44, s41, 0
	s_and_b64 s[42:43], s[14:15], exec
	ds_read_b128 v[82:85], v161
	ds_read_b128 v[94:97], v161 offset:2048
	ds_read_b128 v[102:105], v162
	ds_read_b128 v[110:113], v162 offset:2048
	s_cselect_b32 s47, s37, s44
	s_cselect_b32 s46, s36, s29
	s_add_u32 s29, s38, 0x100
	s_addc_u32 s44, s39, 0
	s_and_b64 s[42:43], s[14:15], exec
	s_cselect_b32 s49, s5, s44
	s_cselect_b32 s48, s4, s29
	s_add_u32 s44, s46, 0x80
	s_addc_u32 s45, s47, 0
	s_add_u32 s42, s48, 0x80
	s_addc_u32 s43, s49, 0
	ds_read_b128 v[58:61], v163
	ds_read_b128 v[66:69], v163 offset:2048
	ds_read_b128 v[62:65], v164
	ds_read_b128 v[70:73], v164 offset:2048
	ds_read_b128 v[74:77], v163 offset:4096
	ds_read_b128 v[86:89], v163 offset:6144
	ds_read_b128 v[78:81], v164 offset:4096
	ds_read_b128 v[90:93], v164 offset:6144
	s_add_u32 s78, s81, 0x80
	s_addc_u32 s79, s82, 0
	s_mov_b32 m0, s70
	s_nop 0
	global_load_lds_dwordx4 v146, s[78:79]
	s_mov_b32 m0, s71
	s_nop 0
	global_load_lds_dwordx4 v150, s[78:79]
	s_waitcnt lgkmcnt(8)
	ds_read_b128 v[142:145], v161 offset:16384
	ds_read_b128 v[166:169], v161 offset:18432
	ds_read_b128 v[170:173], v162 offset:16384
	ds_read_b128 v[174:177], v162 offset:18432
	s_waitcnt vmcnt(8)
	s_waitcnt lgkmcnt(0)
	s_barrier
	s_waitcnt lgkmcnt(0)
	s_waitcnt vmcnt(16)
	v_mov_b32_e32 v1, v0
	v_pk_mul_f32 v[16:17], v[0:1], v[16:17]
	v_pk_mul_f32 v[14:15], v[154:155], v[14:15]
	v_pk_mul_f32 v[12:13], v[0:1], v[12:13]
	v_pk_mul_f32 v[10:11], v[154:155], v[10:11]
	v_pk_mul_f32 v[8:9], v[0:1], v[8:9]
	v_pk_mul_f32 v[6:7], v[154:155], v[6:7]
	v_pk_mul_f32 v[4:5], v[0:1], v[4:5]
	v_pk_mul_f32 v[2:3], v[154:155], v[2:3]
	s_setprio 1
	s_waitcnt lgkmcnt(7)
	v_mfma_f32_16x16x128_f8f6f4 v[18:21], v[82:85], v[58:61], v[14:17] cbsz:4 blgp:4
	s_waitcnt lgkmcnt(5)
	v_mfma_f32_16x16x128_f8f6f4 v[18:21], v[102:105], v[62:65], v[18:21] cbsz:4 blgp:4
	v_mfma_f32_16x16x128_f8f6f4 v[22:25], v[94:97], v[58:61], v[10:13] cbsz:4 blgp:4
	s_nop 0
	v_mfma_f32_16x16x128_f8f6f4 v[22:25], v[110:113], v[62:65], v[22:25] cbsz:4 blgp:4
	v_mfma_f32_16x16x128_f8f6f4 v[26:29], v[82:85], v[66:69], v[14:17] cbsz:4 blgp:4
	s_waitcnt lgkmcnt(4)
	v_mfma_f32_16x16x128_f8f6f4 v[26:29], v[102:105], v[70:73], v[26:29] cbsz:4 blgp:4
	v_mfma_f32_16x16x128_f8f6f4 v[30:33], v[94:97], v[66:69], v[10:13] cbsz:4 blgp:4
	s_nop 0
	v_mfma_f32_16x16x128_f8f6f4 v[30:33], v[110:113], v[70:73], v[30:33] cbsz:4 blgp:4
	s_waitcnt lgkmcnt(3)
	v_mfma_f32_16x16x128_f8f6f4 v[34:37], v[82:85], v[74:77], v[14:17] cbsz:4 blgp:4
	s_waitcnt lgkmcnt(1)
	v_mfma_f32_16x16x128_f8f6f4 v[34:37], v[102:105], v[78:81], v[34:37] cbsz:4 blgp:4
	v_mfma_f32_16x16x128_f8f6f4 v[38:41], v[94:97], v[74:77], v[10:13] cbsz:4 blgp:4
	s_nop 0
	v_mfma_f32_16x16x128_f8f6f4 v[38:41], v[110:113], v[78:81], v[38:41] cbsz:4 blgp:4
	v_mfma_f32_16x16x128_f8f6f4 v[42:45], v[82:85], v[86:89], v[14:17] cbsz:4 blgp:4
	s_waitcnt lgkmcnt(0)
	v_mfma_f32_16x16x128_f8f6f4 v[42:45], v[102:105], v[90:93], v[42:45] cbsz:4 blgp:4
	v_mfma_f32_16x16x128_f8f6f4 v[46:49], v[94:97], v[86:89], v[10:13] cbsz:4 blgp:4
	s_nop 0
	v_mfma_f32_16x16x128_f8f6f4 v[46:49], v[110:113], v[90:93], v[46:49] cbsz:4 blgp:4
	s_waitcnt lgkmcnt(3)
	v_mfma_f32_16x16x128_f8f6f4 v[50:53], v[142:145], v[58:61], v[6:9] cbsz:4 blgp:4
	s_waitcnt lgkmcnt(1)
	v_mfma_f32_16x16x128_f8f6f4 v[50:53], v[170:173], v[62:65], v[50:53] cbsz:4 blgp:4
	v_mfma_f32_16x16x128_f8f6f4 v[54:57], v[166:169], v[58:61], v[2:5] cbsz:4 blgp:4
	s_waitcnt lgkmcnt(0)
	v_mfma_f32_16x16x128_f8f6f4 v[54:57], v[174:177], v[62:65], v[54:57] cbsz:4 blgp:4
	v_mfma_f32_16x16x128_f8f6f4 v[58:61], v[142:145], v[66:69], v[6:9] cbsz:4 blgp:4
	s_nop 0
	v_mfma_f32_16x16x128_f8f6f4 v[58:61], v[170:173], v[70:73], v[58:61] cbsz:4 blgp:4
	v_mfma_f32_16x16x128_f8f6f4 v[62:65], v[166:169], v[66:69], v[2:5] cbsz:4 blgp:4
	s_nop 0
	v_mfma_f32_16x16x128_f8f6f4 v[62:65], v[174:177], v[70:73], v[62:65] cbsz:4 blgp:4
	v_mfma_f32_16x16x128_f8f6f4 v[66:69], v[142:145], v[74:77], v[6:9] cbsz:4 blgp:4
	s_nop 0
	v_mfma_f32_16x16x128_f8f6f4 v[66:69], v[170:173], v[78:81], v[66:69] cbsz:4 blgp:4
	v_mfma_f32_16x16x128_f8f6f4 v[70:73], v[166:169], v[74:77], v[2:5] cbsz:4 blgp:4
	s_nop 0
	v_mfma_f32_16x16x128_f8f6f4 v[70:73], v[174:177], v[78:81], v[70:73] cbsz:4 blgp:4
	v_mfma_f32_16x16x128_f8f6f4 v[74:77], v[142:145], v[86:89], v[6:9] cbsz:4 blgp:4
	s_nop 0
	v_mfma_f32_16x16x128_f8f6f4 v[74:77], v[170:173], v[90:93], v[74:77] cbsz:4 blgp:4
	v_mfma_f32_16x16x128_f8f6f4 v[78:81], v[166:169], v[86:89], v[2:5] cbsz:4 blgp:4
	s_nop 0
	v_mfma_f32_16x16x128_f8f6f4 v[78:81], v[174:177], v[90:93], v[78:81] cbsz:4 blgp:4
	s_setprio 0
	s_barrier
	s_mov_b32 m0, s55
	s_nop 0
	global_load_lds_dwordx4 v148, s[48:49]
	s_mov_b32 m0, s56
	s_nop 0
	global_load_lds_dwordx4 v152, s[48:49]
	ds_read_b128 v[114:117], v163 offset:16384
	ds_read_b128 v[122:125], v163 offset:18432
	ds_read_b128 v[130:133], v164 offset:16384
	ds_read_b128 v[134:137], v164 offset:18432
	ds_read_b128 v[178:181], v163 offset:20480
	ds_read_b128 v[182:185], v163 offset:22528
	ds_read_b128 v[186:189], v164 offset:20480
	ds_read_b128 v[190:193], v164 offset:22528
	s_mov_b32 m0, s54
	s_nop 0
	global_load_lds_dwordx4 v146, s[46:47]
	s_mov_b32 m0, s57
	s_nop 0
	global_load_lds_dwordx4 v150, s[46:47]
	s_add_u32 s48, s48, s24
	s_addc_u32 s49, s49, s25
	s_mov_b32 m0, s58
	s_nop 0
	global_load_lds_dwordx4 v148, s[48:49]
	s_mov_b32 m0, s59
	s_nop 0
	global_load_lds_dwordx4 v152, s[48:49]
	s_waitcnt vmcnt(8)
	s_waitcnt lgkmcnt(0)
	s_barrier
	s_setprio 1
	s_waitcnt lgkmcnt(7)
	v_mfma_f32_16x16x128_f8f6f4 v[86:89], v[82:85], v[114:117], v[14:17] cbsz:4 blgp:4
	s_waitcnt lgkmcnt(5)
	v_mfma_f32_16x16x128_f8f6f4 v[86:89], v[102:105], v[130:133], v[86:89] cbsz:4 blgp:4
	v_mfma_f32_16x16x128_f8f6f4 v[90:93], v[94:97], v[114:117], v[10:13] cbsz:4 blgp:4
	s_nop 0
	v_mfma_f32_16x16x128_f8f6f4 v[90:93], v[110:113], v[130:133], v[90:93] cbsz:4 blgp:4
	v_mfma_f32_16x16x128_f8f6f4 v[98:101], v[82:85], v[122:125], v[14:17] cbsz:4 blgp:4
	s_waitcnt lgkmcnt(4)
	v_mfma_f32_16x16x128_f8f6f4 v[98:101], v[102:105], v[134:137], v[98:101] cbsz:4 blgp:4
	v_mfma_f32_16x16x128_f8f6f4 v[106:109], v[94:97], v[122:125], v[10:13] cbsz:4 blgp:4
	s_nop 0
	v_mfma_f32_16x16x128_f8f6f4 v[106:109], v[110:113], v[134:137], v[106:109] cbsz:4 blgp:4
	s_waitcnt lgkmcnt(3)
	v_mfma_f32_16x16x128_f8f6f4 v[118:121], v[82:85], v[178:181], v[14:17] cbsz:4 blgp:4
	s_waitcnt lgkmcnt(1)
	v_mfma_f32_16x16x128_f8f6f4 v[118:121], v[102:105], v[186:189], v[118:121] cbsz:4 blgp:4
	v_mfma_f32_16x16x128_f8f6f4 v[126:129], v[94:97], v[178:181], v[10:13] cbsz:4 blgp:4
	s_nop 0
	v_mfma_f32_16x16x128_f8f6f4 v[126:129], v[110:113], v[186:189], v[126:129] cbsz:4 blgp:4
	v_mfma_f32_16x16x128_f8f6f4 v[138:141], v[82:85], v[182:185], v[14:17] cbsz:4 blgp:4
	s_waitcnt lgkmcnt(0)
	v_mfma_f32_16x16x128_f8f6f4 v[138:141], v[102:105], v[190:193], v[138:141] cbsz:4 blgp:4
	v_mfma_f32_16x16x128_f8f6f4 v[82:85], v[94:97], v[182:185], v[10:13] cbsz:4 blgp:4
	s_nop 0
	v_mfma_f32_16x16x128_f8f6f4 v[82:85], v[110:113], v[190:193], v[82:85] cbsz:4 blgp:4
	v_mfma_f32_16x16x128_f8f6f4 v[94:97], v[142:145], v[114:117], v[6:9] cbsz:4 blgp:4
	s_nop 0
	v_mfma_f32_16x16x128_f8f6f4 v[94:97], v[170:173], v[130:133], v[94:97] cbsz:4 blgp:4
	v_mfma_f32_16x16x128_f8f6f4 v[102:105], v[166:169], v[114:117], v[2:5] cbsz:4 blgp:4
	s_nop 0
	v_mfma_f32_16x16x128_f8f6f4 v[102:105], v[174:177], v[130:133], v[102:105] cbsz:4 blgp:4
	v_mfma_f32_16x16x128_f8f6f4 v[110:113], v[142:145], v[122:125], v[6:9] cbsz:4 blgp:4
	s_nop 0
	v_mfma_f32_16x16x128_f8f6f4 v[110:113], v[170:173], v[134:137], v[110:113] cbsz:4 blgp:4
	v_mfma_f32_16x16x128_f8f6f4 v[114:117], v[166:169], v[122:125], v[2:5] cbsz:4 blgp:4
	s_nop 0
	v_mfma_f32_16x16x128_f8f6f4 v[114:117], v[174:177], v[134:137], v[114:117] cbsz:4 blgp:4
	v_mfma_f32_16x16x128_f8f6f4 v[122:125], v[142:145], v[178:181], v[6:9] cbsz:4 blgp:4
	s_nop 0
	v_mfma_f32_16x16x128_f8f6f4 v[122:125], v[170:173], v[186:189], v[122:125] cbsz:4 blgp:4
	v_mfma_f32_16x16x128_f8f6f4 v[130:133], v[166:169], v[178:181], v[2:5] cbsz:4 blgp:4
	s_nop 0
	v_mfma_f32_16x16x128_f8f6f4 v[130:133], v[174:177], v[186:189], v[130:133] cbsz:4 blgp:4
	v_mfma_f32_16x16x128_f8f6f4 v[134:137], v[142:145], v[182:185], v[6:9] cbsz:4 blgp:4
	s_nop 0
	v_mfma_f32_16x16x128_f8f6f4 v[134:137], v[170:173], v[190:193], v[134:137] cbsz:4 blgp:4
	v_mfma_f32_16x16x128_f8f6f4 v[142:145], v[166:169], v[182:185], v[2:5] cbsz:4 blgp:4
	s_nop 0
	v_mfma_f32_16x16x128_f8f6f4 v[142:145], v[174:177], v[190:193], v[142:145] cbsz:4 blgp:4
	s_setprio 0
	s_barrier
	ds_read_b128 v[166:169], v161 offset:32768
	ds_read_b128 v[170:173], v161 offset:34816
	ds_read_b128 v[174:177], v162 offset:32768
	ds_read_b128 v[178:181], v162 offset:34816
	ds_read_b128 v[182:185], v163 offset:32768
	ds_read_b128 v[186:189], v163 offset:34816
	ds_read_b128 v[190:193], v164 offset:32768
	ds_read_b128 v[194:197], v164 offset:34816
	ds_read_b128 v[198:201], v163 offset:36864
	ds_read_b128 v[202:205], v163 offset:38912
	ds_read_b128 v[206:209], v164 offset:36864
	ds_read_b128 v[210:213], v164 offset:38912
	s_add_u32 s46, s46, s22
	s_addc_u32 s47, s47, s23
	s_mov_b32 m0, s60
	s_nop 0
	global_load_lds_dwordx4 v146, s[46:47]
	s_mov_b32 m0, s61
	s_nop 0
	global_load_lds_dwordx4 v150, s[46:47]
	s_waitcnt lgkmcnt(8)
	ds_read_b128 v[214:217], v161 offset:49152
	ds_read_b128 v[218:221], v161 offset:51200
	ds_read_b128 v[222:225], v162 offset:49152
	ds_read_b128 v[226:229], v162 offset:51200
	s_waitcnt vmcnt(8)
	s_waitcnt lgkmcnt(0)
	s_barrier
	s_waitcnt lgkmcnt(0)
	s_setprio 1
	s_waitcnt lgkmcnt(7)
	v_mfma_f32_16x16x128_f8f6f4 v[18:21], v[166:169], v[182:185], v[18:21] cbsz:4 blgp:4
	s_waitcnt lgkmcnt(5)
	v_mfma_f32_16x16x128_f8f6f4 v[18:21], v[174:177], v[190:193], v[18:21] cbsz:4 blgp:4
	v_mfma_f32_16x16x128_f8f6f4 v[22:25], v[170:173], v[182:185], v[22:25] cbsz:4 blgp:4
	s_nop 0
	v_mfma_f32_16x16x128_f8f6f4 v[22:25], v[178:181], v[190:193], v[22:25] cbsz:4 blgp:4
	v_mfma_f32_16x16x128_f8f6f4 v[26:29], v[166:169], v[186:189], v[26:29] cbsz:4 blgp:4
	s_waitcnt lgkmcnt(4)
	v_mfma_f32_16x16x128_f8f6f4 v[26:29], v[174:177], v[194:197], v[26:29] cbsz:4 blgp:4
	v_mfma_f32_16x16x128_f8f6f4 v[30:33], v[170:173], v[186:189], v[30:33] cbsz:4 blgp:4
	s_nop 0
	v_mfma_f32_16x16x128_f8f6f4 v[30:33], v[178:181], v[194:197], v[30:33] cbsz:4 blgp:4
	s_waitcnt lgkmcnt(3)
	v_mfma_f32_16x16x128_f8f6f4 v[34:37], v[166:169], v[198:201], v[34:37] cbsz:4 blgp:4
	s_waitcnt lgkmcnt(1)
	v_mfma_f32_16x16x128_f8f6f4 v[34:37], v[174:177], v[206:209], v[34:37] cbsz:4 blgp:4
	v_mfma_f32_16x16x128_f8f6f4 v[38:41], v[170:173], v[198:201], v[38:41] cbsz:4 blgp:4
	s_nop 0
	v_mfma_f32_16x16x128_f8f6f4 v[38:41], v[178:181], v[206:209], v[38:41] cbsz:4 blgp:4
	v_mfma_f32_16x16x128_f8f6f4 v[42:45], v[166:169], v[202:205], v[42:45] cbsz:4 blgp:4
	s_waitcnt lgkmcnt(0)
	v_mfma_f32_16x16x128_f8f6f4 v[42:45], v[174:177], v[210:213], v[42:45] cbsz:4 blgp:4
	v_mfma_f32_16x16x128_f8f6f4 v[46:49], v[170:173], v[202:205], v[46:49] cbsz:4 blgp:4
	s_nop 0
	v_mfma_f32_16x16x128_f8f6f4 v[46:49], v[178:181], v[210:213], v[46:49] cbsz:4 blgp:4
	s_waitcnt lgkmcnt(3)
	v_mfma_f32_16x16x128_f8f6f4 v[50:53], v[214:217], v[182:185], v[50:53] cbsz:4 blgp:4
	s_waitcnt lgkmcnt(1)
	v_mfma_f32_16x16x128_f8f6f4 v[50:53], v[222:225], v[190:193], v[50:53] cbsz:4 blgp:4
	v_mfma_f32_16x16x128_f8f6f4 v[54:57], v[218:221], v[182:185], v[54:57] cbsz:4 blgp:4
	s_waitcnt lgkmcnt(0)
	v_mfma_f32_16x16x128_f8f6f4 v[54:57], v[226:229], v[190:193], v[54:57] cbsz:4 blgp:4
	v_mfma_f32_16x16x128_f8f6f4 v[58:61], v[214:217], v[186:189], v[58:61] cbsz:4 blgp:4
	s_nop 0
	v_mfma_f32_16x16x128_f8f6f4 v[58:61], v[222:225], v[194:197], v[58:61] cbsz:4 blgp:4
	v_mfma_f32_16x16x128_f8f6f4 v[62:65], v[218:221], v[186:189], v[62:65] cbsz:4 blgp:4
	s_nop 0
	v_mfma_f32_16x16x128_f8f6f4 v[62:65], v[226:229], v[194:197], v[62:65] cbsz:4 blgp:4
	v_mfma_f32_16x16x128_f8f6f4 v[66:69], v[214:217], v[198:201], v[66:69] cbsz:4 blgp:4
	s_nop 0
	v_mfma_f32_16x16x128_f8f6f4 v[66:69], v[222:225], v[206:209], v[66:69] cbsz:4 blgp:4
	v_mfma_f32_16x16x128_f8f6f4 v[70:73], v[218:221], v[198:201], v[70:73] cbsz:4 blgp:4
	s_nop 0
	v_mfma_f32_16x16x128_f8f6f4 v[70:73], v[226:229], v[206:209], v[70:73] cbsz:4 blgp:4
	v_mfma_f32_16x16x128_f8f6f4 v[74:77], v[214:217], v[202:205], v[74:77] cbsz:4 blgp:4
	s_nop 0
	v_mfma_f32_16x16x128_f8f6f4 v[74:77], v[222:225], v[210:213], v[74:77] cbsz:4 blgp:4
	v_mfma_f32_16x16x128_f8f6f4 v[78:81], v[218:221], v[202:205], v[78:81] cbsz:4 blgp:4
	s_nop 0
	v_mfma_f32_16x16x128_f8f6f4 v[78:81], v[226:229], v[210:213], v[78:81] cbsz:4 blgp:4
	s_setprio 0
	s_barrier
	s_mov_b32 m0, s64
	s_nop 0
	global_load_lds_dwordx4 v148, s[42:43]
	s_mov_b32 m0, s65
	s_nop 0
	global_load_lds_dwordx4 v152, s[42:43]
	ds_read_b128 v[182:185], v163 offset:49152
	ds_read_b128 v[186:189], v163 offset:51200
	ds_read_b128 v[190:193], v164 offset:49152
	ds_read_b128 v[194:197], v164 offset:51200
	ds_read_b128 v[198:201], v163 offset:53248
	ds_read_b128 v[202:205], v163 offset:55296
	ds_read_b128 v[206:209], v164 offset:53248
	ds_read_b128 v[210:213], v164 offset:55296
	s_mov_b32 m0, s66
	s_nop 0
	global_load_lds_dwordx4 v146, s[44:45]
	s_mov_b32 m0, s67
	s_nop 0
	global_load_lds_dwordx4 v150, s[44:45]
	s_add_u32 s42, s42, s24
	s_addc_u32 s43, s43, s25
	s_mov_b32 m0, s68
	s_nop 0
	global_load_lds_dwordx4 v148, s[42:43]
	s_mov_b32 m0, s69
	s_nop 0
	global_load_lds_dwordx4 v152, s[42:43]
	s_waitcnt vmcnt(8)
	s_waitcnt lgkmcnt(0)
	s_barrier
	s_setprio 1
	s_waitcnt lgkmcnt(7)
	v_mfma_f32_16x16x128_f8f6f4 v[86:89], v[166:169], v[182:185], v[86:89] cbsz:4 blgp:4
	s_waitcnt lgkmcnt(5)
	v_mfma_f32_16x16x128_f8f6f4 v[86:89], v[174:177], v[190:193], v[86:89] cbsz:4 blgp:4
	v_mfma_f32_16x16x128_f8f6f4 v[90:93], v[170:173], v[182:185], v[90:93] cbsz:4 blgp:4
	s_nop 0
	v_mfma_f32_16x16x128_f8f6f4 v[90:93], v[178:181], v[190:193], v[90:93] cbsz:4 blgp:4
	v_mfma_f32_16x16x128_f8f6f4 v[98:101], v[166:169], v[186:189], v[98:101] cbsz:4 blgp:4
	s_waitcnt lgkmcnt(4)
	v_mfma_f32_16x16x128_f8f6f4 v[98:101], v[174:177], v[194:197], v[98:101] cbsz:4 blgp:4
	v_mfma_f32_16x16x128_f8f6f4 v[106:109], v[170:173], v[186:189], v[106:109] cbsz:4 blgp:4
	s_nop 0
	v_mfma_f32_16x16x128_f8f6f4 v[106:109], v[178:181], v[194:197], v[106:109] cbsz:4 blgp:4
	s_waitcnt lgkmcnt(3)
	v_mfma_f32_16x16x128_f8f6f4 v[118:121], v[166:169], v[198:201], v[118:121] cbsz:4 blgp:4
	s_waitcnt lgkmcnt(1)
	v_mfma_f32_16x16x128_f8f6f4 v[118:121], v[174:177], v[206:209], v[118:121] cbsz:4 blgp:4
	v_mfma_f32_16x16x128_f8f6f4 v[126:129], v[170:173], v[198:201], v[126:129] cbsz:4 blgp:4
	s_nop 0
	v_mfma_f32_16x16x128_f8f6f4 v[126:129], v[178:181], v[206:209], v[126:129] cbsz:4 blgp:4
	v_mfma_f32_16x16x128_f8f6f4 v[138:141], v[166:169], v[202:205], v[138:141] cbsz:4 blgp:4
	s_waitcnt lgkmcnt(0)
	v_mfma_f32_16x16x128_f8f6f4 v[138:141], v[174:177], v[210:213], v[138:141] cbsz:4 blgp:4
	v_mfma_f32_16x16x128_f8f6f4 v[82:85], v[170:173], v[202:205], v[82:85] cbsz:4 blgp:4
	s_nop 0
	v_mfma_f32_16x16x128_f8f6f4 v[82:85], v[178:181], v[210:213], v[82:85] cbsz:4 blgp:4
	v_mfma_f32_16x16x128_f8f6f4 v[94:97], v[214:217], v[182:185], v[94:97] cbsz:4 blgp:4
	s_nop 0
	v_mfma_f32_16x16x128_f8f6f4 v[94:97], v[222:225], v[190:193], v[94:97] cbsz:4 blgp:4
	v_mfma_f32_16x16x128_f8f6f4 v[102:105], v[218:221], v[182:185], v[102:105] cbsz:4 blgp:4
	s_nop 0
	v_mfma_f32_16x16x128_f8f6f4 v[102:105], v[226:229], v[190:193], v[102:105] cbsz:4 blgp:4
	v_mfma_f32_16x16x128_f8f6f4 v[110:113], v[214:217], v[186:189], v[110:113] cbsz:4 blgp:4
	s_nop 0
	v_mfma_f32_16x16x128_f8f6f4 v[110:113], v[222:225], v[194:197], v[110:113] cbsz:4 blgp:4
	v_mfma_f32_16x16x128_f8f6f4 v[114:117], v[218:221], v[186:189], v[114:117] cbsz:4 blgp:4
	s_nop 0
	v_mfma_f32_16x16x128_f8f6f4 v[114:117], v[226:229], v[194:197], v[114:117] cbsz:4 blgp:4
	v_mfma_f32_16x16x128_f8f6f4 v[122:125], v[214:217], v[198:201], v[122:125] cbsz:4 blgp:4
	s_nop 0
	v_mfma_f32_16x16x128_f8f6f4 v[122:125], v[222:225], v[206:209], v[122:125] cbsz:4 blgp:4
	v_mfma_f32_16x16x128_f8f6f4 v[130:133], v[218:221], v[198:201], v[130:133] cbsz:4 blgp:4
	s_nop 0
	v_mfma_f32_16x16x128_f8f6f4 v[130:133], v[226:229], v[206:209], v[130:133] cbsz:4 blgp:4
	v_mfma_f32_16x16x128_f8f6f4 v[134:137], v[214:217], v[202:205], v[134:137] cbsz:4 blgp:4
	s_nop 0
	v_mfma_f32_16x16x128_f8f6f4 v[134:137], v[222:225], v[210:213], v[134:137] cbsz:4 blgp:4
	v_mfma_f32_16x16x128_f8f6f4 v[142:145], v[218:221], v[202:205], v[142:145] cbsz:4 blgp:4
	s_nop 0
	v_mfma_f32_16x16x128_f8f6f4 v[142:145], v[226:229], v[210:213], v[142:145] cbsz:4 blgp:4
	s_setprio 0
	s_andn2_b64 vcc, exec, s[34:35]
	s_barrier
	s_cbranch_vccnz .LBB4_4
	s_ashr_i32 s29, s28, 31
	s_lshl_b64 s[42:43], s[28:29], 10
	s_add_u32 s42, s10, s42
	s_addc_u32 s43, s11, s43
	s_add_u32 s29, s40, 0x200
	s_addc_u32 s78, s41, 0
	s_add_u32 s79, s38, 0x200
	s_addc_u32 s80, s39, 0
	s_add_u32 s38, s81, 0x180
	s_addc_u32 s39, s82, 0
	s_mov_b32 s81, 4
	s_cmp_eq_u32 s63, s81
	s_cselect_b64 s[40:41], -1, 0
	s_cmp_lg_u32 s63, s81
	s_cbranch_scc1 .LBB4_15

.LBB4_15:
	ds_read_b128 v[166:169], v161
	ds_read_b128 v[170:173], v161 offset:2048
	ds_read_b128 v[174:177], v162
	ds_read_b128 v[178:181], v162 offset:2048
	s_and_b64 s[40:41], s[40:41], exec
	s_cselect_b32 s46, s36, s29
	s_cselect_b32 s47, s37, s78
	s_cselect_b32 s49, s5, s80
	s_cselect_b32 s48, s4, s79
	s_add_u32 s44, s46, 0x80
	s_addc_u32 s45, s47, 0
	s_add_u32 s40, s48, 0x80
	s_addc_u32 s41, s49, 0
	ds_read_b128 v[182:185], v163
	ds_read_b128 v[186:189], v163 offset:2048
	ds_read_b128 v[190:193], v164
	ds_read_b128 v[194:197], v164 offset:2048
	ds_read_b128 v[198:201], v163 offset:4096
	ds_read_b128 v[202:205], v163 offset:6144
	ds_read_b128 v[206:209], v164 offset:4096
	ds_read_b128 v[210:213], v164 offset:6144
	s_mov_b32 m0, s70
	s_nop 0
	global_load_lds_dwordx4 v146, s[38:39]
	s_mov_b32 m0, s71
	s_nop 0
	global_load_lds_dwordx4 v150, s[38:39]
	s_waitcnt lgkmcnt(8)
	ds_read_b128 v[214:217], v161 offset:16384
	ds_read_b128 v[218:221], v161 offset:18432
	ds_read_b128 v[222:225], v162 offset:16384
	ds_read_b128 v[226:229], v162 offset:18432
	s_waitcnt vmcnt(8)
	s_waitcnt lgkmcnt(0)
	s_barrier
	s_waitcnt lgkmcnt(0)
	s_setprio 1
	s_waitcnt lgkmcnt(7)
	v_mfma_f32_16x16x128_f8f6f4 v[18:21], v[166:169], v[182:185], v[18:21] cbsz:4 blgp:4
	s_waitcnt lgkmcnt(5)
	v_mfma_f32_16x16x128_f8f6f4 v[18:21], v[174:177], v[190:193], v[18:21] cbsz:4 blgp:4
	v_mfma_f32_16x16x128_f8f6f4 v[22:25], v[170:173], v[182:185], v[22:25] cbsz:4 blgp:4
	s_nop 0
	v_mfma_f32_16x16x128_f8f6f4 v[22:25], v[178:181], v[190:193], v[22:25] cbsz:4 blgp:4
	v_mfma_f32_16x16x128_f8f6f4 v[26:29], v[166:169], v[186:189], v[26:29] cbsz:4 blgp:4
	s_waitcnt lgkmcnt(4)
	v_mfma_f32_16x16x128_f8f6f4 v[26:29], v[174:177], v[194:197], v[26:29] cbsz:4 blgp:4
	v_mfma_f32_16x16x128_f8f6f4 v[30:33], v[170:173], v[186:189], v[30:33] cbsz:4 blgp:4
	s_nop 0
	v_mfma_f32_16x16x128_f8f6f4 v[30:33], v[178:181], v[194:197], v[30:33] cbsz:4 blgp:4
	s_waitcnt lgkmcnt(3)
	v_mfma_f32_16x16x128_f8f6f4 v[34:37], v[166:169], v[198:201], v[34:37] cbsz:4 blgp:4
	s_waitcnt lgkmcnt(1)
	v_mfma_f32_16x16x128_f8f6f4 v[34:37], v[174:177], v[206:209], v[34:37] cbsz:4 blgp:4
	v_mfma_f32_16x16x128_f8f6f4 v[38:41], v[170:173], v[198:201], v[38:41] cbsz:4 blgp:4
	s_nop 0
	v_mfma_f32_16x16x128_f8f6f4 v[38:41], v[178:181], v[206:209], v[38:41] cbsz:4 blgp:4
	v_mfma_f32_16x16x128_f8f6f4 v[42:45], v[166:169], v[202:205], v[42:45] cbsz:4 blgp:4
	s_waitcnt lgkmcnt(0)
	v_mfma_f32_16x16x128_f8f6f4 v[42:45], v[174:177], v[210:213], v[42:45] cbsz:4 blgp:4
	v_mfma_f32_16x16x128_f8f6f4 v[46:49], v[170:173], v[202:205], v[46:49] cbsz:4 blgp:4
	s_nop 0
	v_mfma_f32_16x16x128_f8f6f4 v[46:49], v[178:181], v[210:213], v[46:49] cbsz:4 blgp:4
	s_waitcnt lgkmcnt(3)
	v_mfma_f32_16x16x128_f8f6f4 v[50:53], v[214:217], v[182:185], v[50:53] cbsz:4 blgp:4
	s_waitcnt lgkmcnt(1)
	v_mfma_f32_16x16x128_f8f6f4 v[50:53], v[222:225], v[190:193], v[50:53] cbsz:4 blgp:4
	v_mfma_f32_16x16x128_f8f6f4 v[54:57], v[218:221], v[182:185], v[54:57] cbsz:4 blgp:4
	s_waitcnt lgkmcnt(0)
	v_mfma_f32_16x16x128_f8f6f4 v[54:57], v[226:229], v[190:193], v[54:57] cbsz:4 blgp:4
	v_mfma_f32_16x16x128_f8f6f4 v[58:61], v[214:217], v[186:189], v[58:61] cbsz:4 blgp:4
	s_nop 0
	v_mfma_f32_16x16x128_f8f6f4 v[58:61], v[222:225], v[194:197], v[58:61] cbsz:4 blgp:4
	v_mfma_f32_16x16x128_f8f6f4 v[62:65], v[218:221], v[186:189], v[62:65] cbsz:4 blgp:4
	s_nop 0
	v_mfma_f32_16x16x128_f8f6f4 v[62:65], v[226:229], v[194:197], v[62:65] cbsz:4 blgp:4
	v_mfma_f32_16x16x128_f8f6f4 v[66:69], v[214:217], v[198:201], v[66:69] cbsz:4 blgp:4
	s_nop 0
	v_mfma_f32_16x16x128_f8f6f4 v[66:69], v[222:225], v[206:209], v[66:69] cbsz:4 blgp:4
	v_mfma_f32_16x16x128_f8f6f4 v[70:73], v[218:221], v[198:201], v[70:73] cbsz:4 blgp:4
	s_nop 0
	v_mfma_f32_16x16x128_f8f6f4 v[70:73], v[226:229], v[206:209], v[70:73] cbsz:4 blgp:4
	v_mfma_f32_16x16x128_f8f6f4 v[74:77], v[214:217], v[202:205], v[74:77] cbsz:4 blgp:4
	s_nop 0
	v_mfma_f32_16x16x128_f8f6f4 v[74:77], v[222:225], v[210:213], v[74:77] cbsz:4 blgp:4
	v_mfma_f32_16x16x128_f8f6f4 v[78:81], v[218:221], v[202:205], v[78:81] cbsz:4 blgp:4
	s_nop 0
	v_mfma_f32_16x16x128_f8f6f4 v[78:81], v[226:229], v[210:213], v[78:81] cbsz:4 blgp:4
	s_setprio 0
	s_barrier
	s_mov_b32 m0, s55
	s_nop 0
	global_load_lds_dwordx4 v148, s[48:49]
	s_mov_b32 m0, s56
	s_nop 0
	global_load_lds_dwordx4 v152, s[48:49]
	ds_read_b128 v[182:185], v163 offset:16384
	ds_read_b128 v[186:189], v163 offset:18432
	ds_read_b128 v[190:193], v164 offset:16384
	ds_read_b128 v[194:197], v164 offset:18432
	ds_read_b128 v[198:201], v163 offset:20480
	ds_read_b128 v[202:205], v163 offset:22528
	ds_read_b128 v[206:209], v164 offset:20480
	ds_read_b128 v[210:213], v164 offset:22528
	s_mov_b32 m0, s54
	s_nop 0
	global_load_lds_dwordx4 v146, s[46:47]
	s_mov_b32 m0, s57
	s_nop 0
	global_load_lds_dwordx4 v150, s[46:47]
	s_add_u32 s48, s48, s24
	s_addc_u32 s49, s49, s25
	s_mov_b32 m0, s58
	s_nop 0
	global_load_lds_dwordx4 v148, s[48:49]
	s_mov_b32 m0, s59
	s_nop 0
	global_load_lds_dwordx4 v152, s[48:49]
	s_waitcnt vmcnt(8)
	s_waitcnt lgkmcnt(0)
	s_barrier
	s_setprio 1
	s_waitcnt lgkmcnt(7)
	v_mfma_f32_16x16x128_f8f6f4 v[86:89], v[166:169], v[182:185], v[86:89] cbsz:4 blgp:4
	s_waitcnt lgkmcnt(5)
	v_mfma_f32_16x16x128_f8f6f4 v[86:89], v[174:177], v[190:193], v[86:89] cbsz:4 blgp:4
	v_mfma_f32_16x16x128_f8f6f4 v[90:93], v[170:173], v[182:185], v[90:93] cbsz:4 blgp:4
	s_nop 0
	v_mfma_f32_16x16x128_f8f6f4 v[90:93], v[178:181], v[190:193], v[90:93] cbsz:4 blgp:4
	v_mfma_f32_16x16x128_f8f6f4 v[98:101], v[166:169], v[186:189], v[98:101] cbsz:4 blgp:4
	s_waitcnt lgkmcnt(4)
	v_mfma_f32_16x16x128_f8f6f4 v[98:101], v[174:177], v[194:197], v[98:101] cbsz:4 blgp:4
	v_mfma_f32_16x16x128_f8f6f4 v[106:109], v[170:173], v[186:189], v[106:109] cbsz:4 blgp:4
	s_nop 0
	v_mfma_f32_16x16x128_f8f6f4 v[106:109], v[178:181], v[194:197], v[106:109] cbsz:4 blgp:4
	s_waitcnt lgkmcnt(3)
	v_mfma_f32_16x16x128_f8f6f4 v[118:121], v[166:169], v[198:201], v[118:121] cbsz:4 blgp:4
	s_waitcnt lgkmcnt(1)
	v_mfma_f32_16x16x128_f8f6f4 v[118:121], v[174:177], v[206:209], v[118:121] cbsz:4 blgp:4
	v_mfma_f32_16x16x128_f8f6f4 v[126:129], v[170:173], v[198:201], v[126:129] cbsz:4 blgp:4
	s_nop 0
	v_mfma_f32_16x16x128_f8f6f4 v[126:129], v[178:181], v[206:209], v[126:129] cbsz:4 blgp:4
	v_mfma_f32_16x16x128_f8f6f4 v[138:141], v[166:169], v[202:205], v[138:141] cbsz:4 blgp:4
	s_waitcnt lgkmcnt(0)
	v_mfma_f32_16x16x128_f8f6f4 v[138:141], v[174:177], v[210:213], v[138:141] cbsz:4 blgp:4
	v_mfma_f32_16x16x128_f8f6f4 v[82:85], v[170:173], v[202:205], v[82:85] cbsz:4 blgp:4
	s_nop 0
	v_mfma_f32_16x16x128_f8f6f4 v[82:85], v[178:181], v[210:213], v[82:85] cbsz:4 blgp:4
	v_mfma_f32_16x16x128_f8f6f4 v[94:97], v[214:217], v[182:185], v[94:97] cbsz:4 blgp:4
	s_nop 0
	v_mfma_f32_16x16x128_f8f6f4 v[94:97], v[222:225], v[190:193], v[94:97] cbsz:4 blgp:4
	v_mfma_f32_16x16x128_f8f6f4 v[102:105], v[218:221], v[182:185], v[102:105] cbsz:4 blgp:4
	s_nop 0
	v_mfma_f32_16x16x128_f8f6f4 v[102:105], v[226:229], v[190:193], v[102:105] cbsz:4 blgp:4
	v_mfma_f32_16x16x128_f8f6f4 v[110:113], v[214:217], v[186:189], v[110:113] cbsz:4 blgp:4
	s_nop 0
	v_mfma_f32_16x16x128_f8f6f4 v[110:113], v[222:225], v[194:197], v[110:113] cbsz:4 blgp:4
	v_mfma_f32_16x16x128_f8f6f4 v[114:117], v[218:221], v[186:189], v[114:117] cbsz:4 blgp:4
	s_nop 0
	v_mfma_f32_16x16x128_f8f6f4 v[114:117], v[226:229], v[194:197], v[114:117] cbsz:4 blgp:4
	v_mfma_f32_16x16x128_f8f6f4 v[122:125], v[214:217], v[198:201], v[122:125] cbsz:4 blgp:4
	s_nop 0
	v_mfma_f32_16x16x128_f8f6f4 v[122:125], v[222:225], v[206:209], v[122:125] cbsz:4 blgp:4
	v_mfma_f32_16x16x128_f8f6f4 v[130:133], v[218:221], v[198:201], v[130:133] cbsz:4 blgp:4
	s_nop 0
	v_mfma_f32_16x16x128_f8f6f4 v[130:133], v[226:229], v[206:209], v[130:133] cbsz:4 blgp:4
	v_mfma_f32_16x16x128_f8f6f4 v[134:137], v[214:217], v[202:205], v[134:137] cbsz:4 blgp:4
	s_nop 0
	v_mfma_f32_16x16x128_f8f6f4 v[134:137], v[222:225], v[210:213], v[134:137] cbsz:4 blgp:4
	v_mfma_f32_16x16x128_f8f6f4 v[142:145], v[218:221], v[202:205], v[142:145] cbsz:4 blgp:4
	s_nop 0
	v_mfma_f32_16x16x128_f8f6f4 v[142:145], v[226:229], v[210:213], v[142:145] cbsz:4 blgp:4
	s_setprio 0
	s_barrier
	ds_read_b128 v[166:169], v161 offset:32768
	ds_read_b128 v[170:173], v161 offset:34816
	ds_read_b128 v[174:177], v162 offset:32768
	ds_read_b128 v[178:181], v162 offset:34816
	ds_read_b128 v[182:185], v163 offset:32768
	ds_read_b128 v[186:189], v163 offset:34816
	ds_read_b128 v[190:193], v164 offset:32768
	ds_read_b128 v[194:197], v164 offset:34816
	ds_read_b128 v[198:201], v163 offset:36864
	ds_read_b128 v[202:205], v163 offset:38912
	ds_read_b128 v[206:209], v164 offset:36864
	ds_read_b128 v[210:213], v164 offset:38912
	s_add_u32 s46, s46, s22
	s_addc_u32 s47, s47, s23
	s_mov_b32 m0, s60
	s_nop 0
	global_load_lds_dwordx4 v146, s[46:47]
	s_mov_b32 m0, s61
	s_nop 0
	global_load_lds_dwordx4 v150, s[46:47]
	s_waitcnt lgkmcnt(8)
	ds_read_b128 v[214:217], v161 offset:49152
	ds_read_b128 v[218:221], v161 offset:51200
	ds_read_b128 v[222:225], v162 offset:49152
	ds_read_b128 v[226:229], v162 offset:51200
	s_waitcnt vmcnt(8)
	s_waitcnt lgkmcnt(0)
	s_barrier
	s_waitcnt lgkmcnt(0)
	s_setprio 1
	s_waitcnt lgkmcnt(7)
	v_mfma_f32_16x16x128_f8f6f4 v[18:21], v[166:169], v[182:185], v[18:21] cbsz:4 blgp:4
	s_waitcnt lgkmcnt(5)
	v_mfma_f32_16x16x128_f8f6f4 v[18:21], v[174:177], v[190:193], v[18:21] cbsz:4 blgp:4
	v_mfma_f32_16x16x128_f8f6f4 v[22:25], v[170:173], v[182:185], v[22:25] cbsz:4 blgp:4
	s_nop 0
	v_mfma_f32_16x16x128_f8f6f4 v[22:25], v[178:181], v[190:193], v[22:25] cbsz:4 blgp:4
	v_mfma_f32_16x16x128_f8f6f4 v[26:29], v[166:169], v[186:189], v[26:29] cbsz:4 blgp:4
	s_waitcnt lgkmcnt(4)
	v_mfma_f32_16x16x128_f8f6f4 v[26:29], v[174:177], v[194:197], v[26:29] cbsz:4 blgp:4
	v_mfma_f32_16x16x128_f8f6f4 v[30:33], v[170:173], v[186:189], v[30:33] cbsz:4 blgp:4
	s_nop 0
	v_mfma_f32_16x16x128_f8f6f4 v[30:33], v[178:181], v[194:197], v[30:33] cbsz:4 blgp:4
	s_waitcnt lgkmcnt(3)
	v_mfma_f32_16x16x128_f8f6f4 v[34:37], v[166:169], v[198:201], v[34:37] cbsz:4 blgp:4
	s_waitcnt lgkmcnt(1)
	v_mfma_f32_16x16x128_f8f6f4 v[34:37], v[174:177], v[206:209], v[34:37] cbsz:4 blgp:4
	v_mfma_f32_16x16x128_f8f6f4 v[38:41], v[170:173], v[198:201], v[38:41] cbsz:4 blgp:4
	s_nop 0
	v_mfma_f32_16x16x128_f8f6f4 v[38:41], v[178:181], v[206:209], v[38:41] cbsz:4 blgp:4
	v_mfma_f32_16x16x128_f8f6f4 v[42:45], v[166:169], v[202:205], v[42:45] cbsz:4 blgp:4
	s_waitcnt lgkmcnt(0)
	v_mfma_f32_16x16x128_f8f6f4 v[42:45], v[174:177], v[210:213], v[42:45] cbsz:4 blgp:4
	v_mfma_f32_16x16x128_f8f6f4 v[46:49], v[170:173], v[202:205], v[46:49] cbsz:4 blgp:4
	s_nop 0
	v_mfma_f32_16x16x128_f8f6f4 v[46:49], v[178:181], v[210:213], v[46:49] cbsz:4 blgp:4
	s_waitcnt lgkmcnt(3)
	v_mfma_f32_16x16x128_f8f6f4 v[50:53], v[214:217], v[182:185], v[50:53] cbsz:4 blgp:4
	s_waitcnt lgkmcnt(1)
	v_mfma_f32_16x16x128_f8f6f4 v[50:53], v[222:225], v[190:193], v[50:53] cbsz:4 blgp:4
	v_mfma_f32_16x16x128_f8f6f4 v[54:57], v[218:221], v[182:185], v[54:57] cbsz:4 blgp:4
	s_waitcnt lgkmcnt(0)
	v_mfma_f32_16x16x128_f8f6f4 v[54:57], v[226:229], v[190:193], v[54:57] cbsz:4 blgp:4
	v_mfma_f32_16x16x128_f8f6f4 v[58:61], v[214:217], v[186:189], v[58:61] cbsz:4 blgp:4
	s_nop 0
	v_mfma_f32_16x16x128_f8f6f4 v[58:61], v[222:225], v[194:197], v[58:61] cbsz:4 blgp:4
	v_mfma_f32_16x16x128_f8f6f4 v[62:65], v[218:221], v[186:189], v[62:65] cbsz:4 blgp:4
	s_nop 0
	v_mfma_f32_16x16x128_f8f6f4 v[62:65], v[226:229], v[194:197], v[62:65] cbsz:4 blgp:4
	v_mfma_f32_16x16x128_f8f6f4 v[66:69], v[214:217], v[198:201], v[66:69] cbsz:4 blgp:4
	s_nop 0
	v_mfma_f32_16x16x128_f8f6f4 v[66:69], v[222:225], v[206:209], v[66:69] cbsz:4 blgp:4
	v_mfma_f32_16x16x128_f8f6f4 v[70:73], v[218:221], v[198:201], v[70:73] cbsz:4 blgp:4
	s_nop 0
	v_mfma_f32_16x16x128_f8f6f4 v[70:73], v[226:229], v[206:209], v[70:73] cbsz:4 blgp:4
	v_mfma_f32_16x16x128_f8f6f4 v[74:77], v[214:217], v[202:205], v[74:77] cbsz:4 blgp:4
	s_nop 0
	v_mfma_f32_16x16x128_f8f6f4 v[74:77], v[222:225], v[210:213], v[74:77] cbsz:4 blgp:4
	v_mfma_f32_16x16x128_f8f6f4 v[78:81], v[218:221], v[202:205], v[78:81] cbsz:4 blgp:4
	s_nop 0
	v_mfma_f32_16x16x128_f8f6f4 v[78:81], v[226:229], v[210:213], v[78:81] cbsz:4 blgp:4
	s_setprio 0
	s_barrier
	s_mov_b32 m0, s64
	s_nop 0
	global_load_lds_dwordx4 v148, s[40:41]
	s_mov_b32 m0, s65
	s_nop 0
	global_load_lds_dwordx4 v152, s[40:41]
	ds_read_b128 v[182:185], v163 offset:49152
	ds_read_b128 v[186:189], v163 offset:51200
	ds_read_b128 v[190:193], v164 offset:49152
	ds_read_b128 v[194:197], v164 offset:51200
	ds_read_b128 v[198:201], v163 offset:53248
	ds_read_b128 v[202:205], v163 offset:55296
	ds_read_b128 v[206:209], v164 offset:53248
	ds_read_b128 v[210:213], v164 offset:55296
	s_mov_b32 m0, s66
	s_nop 0
	global_load_lds_dwordx4 v146, s[44:45]
	s_mov_b32 m0, s67
	s_nop 0
	global_load_lds_dwordx4 v150, s[44:45]
	s_add_u32 s40, s40, s24
	s_addc_u32 s41, s41, s25
	s_mov_b32 m0, s68
	s_nop 0
	global_load_lds_dwordx4 v148, s[40:41]
	s_mov_b32 m0, s69
	s_nop 0
	global_load_lds_dwordx4 v152, s[40:41]
	s_waitcnt vmcnt(8)
	s_waitcnt lgkmcnt(0)
	s_barrier
	s_setprio 1
	s_waitcnt lgkmcnt(7)
	v_mfma_f32_16x16x128_f8f6f4 v[86:89], v[166:169], v[182:185], v[86:89] cbsz:4 blgp:4
	s_waitcnt lgkmcnt(5)
	v_mfma_f32_16x16x128_f8f6f4 v[86:89], v[174:177], v[190:193], v[86:89] cbsz:4 blgp:4
	v_mfma_f32_16x16x128_f8f6f4 v[90:93], v[170:173], v[182:185], v[90:93] cbsz:4 blgp:4
	s_nop 0
	v_mfma_f32_16x16x128_f8f6f4 v[90:93], v[178:181], v[190:193], v[90:93] cbsz:4 blgp:4
	v_mfma_f32_16x16x128_f8f6f4 v[98:101], v[166:169], v[186:189], v[98:101] cbsz:4 blgp:4
	s_waitcnt lgkmcnt(4)
	v_mfma_f32_16x16x128_f8f6f4 v[98:101], v[174:177], v[194:197], v[98:101] cbsz:4 blgp:4
	v_mfma_f32_16x16x128_f8f6f4 v[106:109], v[170:173], v[186:189], v[106:109] cbsz:4 blgp:4
	s_nop 0
	v_mfma_f32_16x16x128_f8f6f4 v[106:109], v[178:181], v[194:197], v[106:109] cbsz:4 blgp:4
	s_waitcnt lgkmcnt(3)
	v_mfma_f32_16x16x128_f8f6f4 v[118:121], v[166:169], v[198:201], v[118:121] cbsz:4 blgp:4
	s_waitcnt lgkmcnt(1)
	v_mfma_f32_16x16x128_f8f6f4 v[118:121], v[174:177], v[206:209], v[118:121] cbsz:4 blgp:4
	v_mfma_f32_16x16x128_f8f6f4 v[126:129], v[170:173], v[198:201], v[126:129] cbsz:4 blgp:4
	s_nop 0
	v_mfma_f32_16x16x128_f8f6f4 v[126:129], v[178:181], v[206:209], v[126:129] cbsz:4 blgp:4
	v_mfma_f32_16x16x128_f8f6f4 v[138:141], v[166:169], v[202:205], v[138:141] cbsz:4 blgp:4
	s_waitcnt lgkmcnt(0)
	v_mfma_f32_16x16x128_f8f6f4 v[138:141], v[174:177], v[210:213], v[138:141] cbsz:4 blgp:4
	v_mfma_f32_16x16x128_f8f6f4 v[82:85], v[170:173], v[202:205], v[82:85] cbsz:4 blgp:4
	s_nop 0
	v_mfma_f32_16x16x128_f8f6f4 v[82:85], v[178:181], v[210:213], v[82:85] cbsz:4 blgp:4
	v_mfma_f32_16x16x128_f8f6f4 v[94:97], v[214:217], v[182:185], v[94:97] cbsz:4 blgp:4
	s_nop 0
	v_mfma_f32_16x16x128_f8f6f4 v[94:97], v[222:225], v[190:193], v[94:97] cbsz:4 blgp:4
	v_mfma_f32_16x16x128_f8f6f4 v[102:105], v[218:221], v[182:185], v[102:105] cbsz:4 blgp:4
	s_nop 0
	v_mfma_f32_16x16x128_f8f6f4 v[102:105], v[226:229], v[190:193], v[102:105] cbsz:4 blgp:4
	v_mfma_f32_16x16x128_f8f6f4 v[110:113], v[214:217], v[186:189], v[110:113] cbsz:4 blgp:4
	s_nop 0
	v_mfma_f32_16x16x128_f8f6f4 v[110:113], v[222:225], v[194:197], v[110:113] cbsz:4 blgp:4
	v_mfma_f32_16x16x128_f8f6f4 v[114:117], v[218:221], v[186:189], v[114:117] cbsz:4 blgp:4
	s_nop 0
	v_mfma_f32_16x16x128_f8f6f4 v[114:117], v[226:229], v[194:197], v[114:117] cbsz:4 blgp:4
	v_mfma_f32_16x16x128_f8f6f4 v[122:125], v[214:217], v[198:201], v[122:125] cbsz:4 blgp:4
	s_nop 0
	v_mfma_f32_16x16x128_f8f6f4 v[122:125], v[222:225], v[206:209], v[122:125] cbsz:4 blgp:4
	v_mfma_f32_16x16x128_f8f6f4 v[130:133], v[218:221], v[198:201], v[130:133] cbsz:4 blgp:4
	s_nop 0
	v_mfma_f32_16x16x128_f8f6f4 v[130:133], v[226:229], v[206:209], v[130:133] cbsz:4 blgp:4
	v_mfma_f32_16x16x128_f8f6f4 v[134:137], v[214:217], v[202:205], v[134:137] cbsz:4 blgp:4
	s_nop 0
	v_mfma_f32_16x16x128_f8f6f4 v[134:137], v[222:225], v[210:213], v[134:137] cbsz:4 blgp:4
	v_mfma_f32_16x16x128_f8f6f4 v[142:145], v[218:221], v[202:205], v[142:145] cbsz:4 blgp:4
	s_nop 0
	v_mfma_f32_16x16x128_f8f6f4 v[142:145], v[226:229], v[210:213], v[142:145] cbsz:4 blgp:4
	s_setprio 0
	s_add_i32 s40, s81, 2
	s_add_u32 s29, s29, 0x100
	s_addc_u32 s78, s78, 0
	s_add_u32 s79, s79, 0x100
	s_addc_u32 s80, s80, 0
	s_add_u32 s38, s38, 0x100
	s_addc_u32 s39, s39, 0
	s_cmp_ge_i32 s81, s63
	s_barrier
	s_cbranch_scc1 .LBB4_4
	s_mov_b32 s81, s40
	s_cmp_eq_u32 s63, s81
	s_cselect_b64 s[40:41], -1, 0
	s_cmp_lg_u32 s63, s81
	s_cbranch_scc0 .LBB4_14
	s_branch .LBB4_15

.Lrs_a_5:
	s_add_u32 s82, s42, s22
	s_addc_u32 s83, s43, s23
	s_add_u32 s29, s42, 0x100
	s_addc_u32 s46, s43, 0
	s_and_b64 s[44:45], s[14:15], exec
	ds_read_b128 v[82:85], v163
	ds_read_b128 v[94:97], v163 offset:2048
	ds_read_b128 v[102:105], v164
	ds_read_b128 v[110:113], v164 offset:2048
	s_cselect_b32 s49, s39, s46
	s_cselect_b32 s48, s38, s29
	s_add_u32 s29, s40, 0x100
	s_addc_u32 s46, s41, 0
	s_and_b64 s[44:45], s[14:15], exec
	s_cselect_b32 s51, s5, s46
	s_cselect_b32 s50, s4, s29
	s_add_u32 s46, s48, 0x80
	s_addc_u32 s47, s49, 0
	s_add_u32 s44, s50, 0x80
	s_addc_u32 s45, s51, 0
	ds_read_b128 v[58:61], v165
	ds_read_b128 v[66:69], v165 offset:2048
	ds_read_b128 v[62:65], v166
	ds_read_b128 v[70:73], v166 offset:2048
	ds_read_b128 v[74:77], v165 offset:4096
	ds_read_b128 v[86:89], v165 offset:6144
	ds_read_b128 v[78:81], v166 offset:4096
	ds_read_b128 v[90:93], v166 offset:6144
	s_add_u32 s80, s82, 0x80
	s_addc_u32 s81, s83, 0
	s_mov_b32 m0, s71
	s_nop 0
	global_load_lds_dwordx4 v146, s[80:81]
	s_mov_b32 m0, s72
	s_nop 0
	global_load_lds_dwordx4 v150, s[80:81]
	s_waitcnt lgkmcnt(8)
	ds_read_b128 v[142:145], v163 offset:16384
	ds_read_b128 v[156:159], v163 offset:18432
	ds_read_b128 v[168:171], v164 offset:16384
	ds_read_b128 v[172:175], v164 offset:18432
	s_waitcnt vmcnt(8)
	s_waitcnt lgkmcnt(0)
	s_barrier
	s_waitcnt lgkmcnt(0)
	s_waitcnt vmcnt(16)
	v_mov_b32_e32 v1, v0
	v_pk_mul_f32 v[16:17], v[0:1], v[16:17]
	v_pk_mul_f32 v[14:15], v[154:155], v[14:15]
	v_pk_mul_f32 v[12:13], v[0:1], v[12:13]
	v_pk_mul_f32 v[10:11], v[154:155], v[10:11]
	v_pk_mul_f32 v[8:9], v[0:1], v[8:9]
	v_pk_mul_f32 v[6:7], v[154:155], v[6:7]
	v_pk_mul_f32 v[4:5], v[0:1], v[4:5]
	v_pk_mul_f32 v[2:3], v[154:155], v[2:3]
	s_setprio 1
	s_waitcnt lgkmcnt(7)
	v_mfma_f32_16x16x128_f8f6f4 v[18:21], v[82:85], v[58:61], v[14:17] cbsz:4 blgp:4
	s_waitcnt lgkmcnt(5)
	v_mfma_f32_16x16x128_f8f6f4 v[18:21], v[102:105], v[62:65], v[18:21] cbsz:4 blgp:4
	v_mfma_f32_16x16x128_f8f6f4 v[22:25], v[94:97], v[58:61], v[10:13] cbsz:4 blgp:4
	s_nop 0
	v_mfma_f32_16x16x128_f8f6f4 v[22:25], v[110:113], v[62:65], v[22:25] cbsz:4 blgp:4
	v_mfma_f32_16x16x128_f8f6f4 v[26:29], v[82:85], v[66:69], v[14:17] cbsz:4 blgp:4
	s_waitcnt lgkmcnt(4)
	v_mfma_f32_16x16x128_f8f6f4 v[26:29], v[102:105], v[70:73], v[26:29] cbsz:4 blgp:4
	v_mfma_f32_16x16x128_f8f6f4 v[30:33], v[94:97], v[66:69], v[10:13] cbsz:4 blgp:4
	s_nop 0
	v_mfma_f32_16x16x128_f8f6f4 v[30:33], v[110:113], v[70:73], v[30:33] cbsz:4 blgp:4
	s_waitcnt lgkmcnt(3)
	v_mfma_f32_16x16x128_f8f6f4 v[34:37], v[82:85], v[74:77], v[14:17] cbsz:4 blgp:4
	s_waitcnt lgkmcnt(1)
	v_mfma_f32_16x16x128_f8f6f4 v[34:37], v[102:105], v[78:81], v[34:37] cbsz:4 blgp:4
	v_mfma_f32_16x16x128_f8f6f4 v[38:41], v[94:97], v[74:77], v[10:13] cbsz:4 blgp:4
	s_nop 0
	v_mfma_f32_16x16x128_f8f6f4 v[38:41], v[110:113], v[78:81], v[38:41] cbsz:4 blgp:4
	v_mfma_f32_16x16x128_f8f6f4 v[42:45], v[82:85], v[86:89], v[14:17] cbsz:4 blgp:4
	s_waitcnt lgkmcnt(0)
	v_mfma_f32_16x16x128_f8f6f4 v[42:45], v[102:105], v[90:93], v[42:45] cbsz:4 blgp:4
	v_mfma_f32_16x16x128_f8f6f4 v[46:49], v[94:97], v[86:89], v[10:13] cbsz:4 blgp:4
	s_nop 0
	v_mfma_f32_16x16x128_f8f6f4 v[46:49], v[110:113], v[90:93], v[46:49] cbsz:4 blgp:4
	s_waitcnt lgkmcnt(3)
	v_mfma_f32_16x16x128_f8f6f4 v[50:53], v[142:145], v[58:61], v[6:9] cbsz:4 blgp:4
	s_waitcnt lgkmcnt(1)
	v_mfma_f32_16x16x128_f8f6f4 v[50:53], v[168:171], v[62:65], v[50:53] cbsz:4 blgp:4
	v_mfma_f32_16x16x128_f8f6f4 v[54:57], v[156:159], v[58:61], v[2:5] cbsz:4 blgp:4
	s_waitcnt lgkmcnt(0)
	v_mfma_f32_16x16x128_f8f6f4 v[54:57], v[172:175], v[62:65], v[54:57] cbsz:4 blgp:4
	v_mfma_f32_16x16x128_f8f6f4 v[58:61], v[142:145], v[66:69], v[6:9] cbsz:4 blgp:4
	s_nop 0
	v_mfma_f32_16x16x128_f8f6f4 v[58:61], v[168:171], v[70:73], v[58:61] cbsz:4 blgp:4
	v_mfma_f32_16x16x128_f8f6f4 v[62:65], v[156:159], v[66:69], v[2:5] cbsz:4 blgp:4
	s_nop 0
	v_mfma_f32_16x16x128_f8f6f4 v[62:65], v[172:175], v[70:73], v[62:65] cbsz:4 blgp:4
	v_mfma_f32_16x16x128_f8f6f4 v[66:69], v[142:145], v[74:77], v[6:9] cbsz:4 blgp:4
	s_nop 0
	v_mfma_f32_16x16x128_f8f6f4 v[66:69], v[168:171], v[78:81], v[66:69] cbsz:4 blgp:4
	v_mfma_f32_16x16x128_f8f6f4 v[70:73], v[156:159], v[74:77], v[2:5] cbsz:4 blgp:4
	s_nop 0
	v_mfma_f32_16x16x128_f8f6f4 v[70:73], v[172:175], v[78:81], v[70:73] cbsz:4 blgp:4
	v_mfma_f32_16x16x128_f8f6f4 v[74:77], v[142:145], v[86:89], v[6:9] cbsz:4 blgp:4
	s_nop 0
	v_mfma_f32_16x16x128_f8f6f4 v[74:77], v[168:171], v[90:93], v[74:77] cbsz:4 blgp:4
	v_mfma_f32_16x16x128_f8f6f4 v[78:81], v[156:159], v[86:89], v[2:5] cbsz:4 blgp:4
	s_nop 0
	v_mfma_f32_16x16x128_f8f6f4 v[78:81], v[172:175], v[90:93], v[78:81] cbsz:4 blgp:4
	s_setprio 0
	s_barrier
	s_mov_b32 m0, s56
	s_nop 0
	global_load_lds_dwordx4 v148, s[50:51]
	s_mov_b32 m0, s57
	s_nop 0
	global_load_lds_dwordx4 v152, s[50:51]
	ds_read_b128 v[114:117], v165 offset:16384
	ds_read_b128 v[122:125], v165 offset:18432
	ds_read_b128 v[130:133], v166 offset:16384
	ds_read_b128 v[134:137], v166 offset:18432
	ds_read_b128 v[176:179], v165 offset:20480
	ds_read_b128 v[180:183], v165 offset:22528
	ds_read_b128 v[184:187], v166 offset:20480
	ds_read_b128 v[188:191], v166 offset:22528
	s_mov_b32 m0, s55
	s_nop 0
	global_load_lds_dwordx4 v146, s[48:49]
	s_mov_b32 m0, s58
	s_nop 0
	global_load_lds_dwordx4 v150, s[48:49]
	s_add_u32 s50, s50, s24
	s_addc_u32 s51, s51, s25
	s_mov_b32 m0, s59
	s_nop 0
	global_load_lds_dwordx4 v148, s[50:51]
	s_mov_b32 m0, s60
	s_nop 0
	global_load_lds_dwordx4 v152, s[50:51]
	s_waitcnt vmcnt(8)
	s_waitcnt lgkmcnt(0)
	s_barrier
	s_setprio 1
	s_waitcnt lgkmcnt(7)
	v_mfma_f32_16x16x128_f8f6f4 v[86:89], v[82:85], v[114:117], v[14:17] cbsz:4 blgp:4
	s_waitcnt lgkmcnt(5)
	v_mfma_f32_16x16x128_f8f6f4 v[86:89], v[102:105], v[130:133], v[86:89] cbsz:4 blgp:4
	v_mfma_f32_16x16x128_f8f6f4 v[90:93], v[94:97], v[114:117], v[10:13] cbsz:4 blgp:4
	s_nop 0
	v_mfma_f32_16x16x128_f8f6f4 v[90:93], v[110:113], v[130:133], v[90:93] cbsz:4 blgp:4
	v_mfma_f32_16x16x128_f8f6f4 v[98:101], v[82:85], v[122:125], v[14:17] cbsz:4 blgp:4
	s_waitcnt lgkmcnt(4)
	v_mfma_f32_16x16x128_f8f6f4 v[98:101], v[102:105], v[134:137], v[98:101] cbsz:4 blgp:4
	v_mfma_f32_16x16x128_f8f6f4 v[106:109], v[94:97], v[122:125], v[10:13] cbsz:4 blgp:4
	s_nop 0
	v_mfma_f32_16x16x128_f8f6f4 v[106:109], v[110:113], v[134:137], v[106:109] cbsz:4 blgp:4
	s_waitcnt lgkmcnt(3)
	v_mfma_f32_16x16x128_f8f6f4 v[118:121], v[82:85], v[176:179], v[14:17] cbsz:4 blgp:4
	s_waitcnt lgkmcnt(1)
	v_mfma_f32_16x16x128_f8f6f4 v[118:121], v[102:105], v[184:187], v[118:121] cbsz:4 blgp:4
	v_mfma_f32_16x16x128_f8f6f4 v[126:129], v[94:97], v[176:179], v[10:13] cbsz:4 blgp:4
	s_nop 0
	v_mfma_f32_16x16x128_f8f6f4 v[126:129], v[110:113], v[184:187], v[126:129] cbsz:4 blgp:4
	v_mfma_f32_16x16x128_f8f6f4 v[138:141], v[82:85], v[180:183], v[14:17] cbsz:4 blgp:4
	s_waitcnt lgkmcnt(0)
	v_mfma_f32_16x16x128_f8f6f4 v[138:141], v[102:105], v[188:191], v[138:141] cbsz:4 blgp:4
	v_mfma_f32_16x16x128_f8f6f4 v[82:85], v[94:97], v[180:183], v[10:13] cbsz:4 blgp:4
	s_nop 0
	v_mfma_f32_16x16x128_f8f6f4 v[82:85], v[110:113], v[188:191], v[82:85] cbsz:4 blgp:4
	v_mfma_f32_16x16x128_f8f6f4 v[94:97], v[142:145], v[114:117], v[6:9] cbsz:4 blgp:4
	s_nop 0
	v_mfma_f32_16x16x128_f8f6f4 v[94:97], v[168:171], v[130:133], v[94:97] cbsz:4 blgp:4
	v_mfma_f32_16x16x128_f8f6f4 v[102:105], v[156:159], v[114:117], v[2:5] cbsz:4 blgp:4
	s_nop 0
	v_mfma_f32_16x16x128_f8f6f4 v[102:105], v[172:175], v[130:133], v[102:105] cbsz:4 blgp:4
	v_mfma_f32_16x16x128_f8f6f4 v[110:113], v[142:145], v[122:125], v[6:9] cbsz:4 blgp:4
	s_nop 0
	v_mfma_f32_16x16x128_f8f6f4 v[110:113], v[168:171], v[134:137], v[110:113] cbsz:4 blgp:4
	v_mfma_f32_16x16x128_f8f6f4 v[114:117], v[156:159], v[122:125], v[2:5] cbsz:4 blgp:4
	s_nop 0
	v_mfma_f32_16x16x128_f8f6f4 v[114:117], v[172:175], v[134:137], v[114:117] cbsz:4 blgp:4
	v_mfma_f32_16x16x128_f8f6f4 v[122:125], v[142:145], v[176:179], v[6:9] cbsz:4 blgp:4
	s_nop 0
	v_mfma_f32_16x16x128_f8f6f4 v[122:125], v[168:171], v[184:187], v[122:125] cbsz:4 blgp:4
	v_mfma_f32_16x16x128_f8f6f4 v[130:133], v[156:159], v[176:179], v[2:5] cbsz:4 blgp:4
	s_nop 0
	v_mfma_f32_16x16x128_f8f6f4 v[130:133], v[172:175], v[184:187], v[130:133] cbsz:4 blgp:4
	v_mfma_f32_16x16x128_f8f6f4 v[134:137], v[142:145], v[180:183], v[6:9] cbsz:4 blgp:4
	s_nop 0
	v_mfma_f32_16x16x128_f8f6f4 v[134:137], v[168:171], v[188:191], v[134:137] cbsz:4 blgp:4
	v_mfma_f32_16x16x128_f8f6f4 v[142:145], v[156:159], v[180:183], v[2:5] cbsz:4 blgp:4
	s_nop 0
	v_mfma_f32_16x16x128_f8f6f4 v[142:145], v[172:175], v[188:191], v[142:145] cbsz:4 blgp:4
	s_setprio 0
	s_barrier
	ds_read_b128 v[156:159], v163 offset:32768
	ds_read_b128 v[168:171], v163 offset:34816
	ds_read_b128 v[172:175], v164 offset:32768
	ds_read_b128 v[176:179], v164 offset:34816
	ds_read_b128 v[180:183], v165 offset:32768
	ds_read_b128 v[184:187], v165 offset:34816
	ds_read_b128 v[188:191], v166 offset:32768
	ds_read_b128 v[192:195], v166 offset:34816
	ds_read_b128 v[196:199], v165 offset:36864
	ds_read_b128 v[200:203], v165 offset:38912
	ds_read_b128 v[204:207], v166 offset:36864
	ds_read_b128 v[208:211], v166 offset:38912
	s_add_u32 s48, s48, s22
	s_addc_u32 s49, s49, s23
	s_mov_b32 m0, s61
	s_nop 0
	global_load_lds_dwordx4 v146, s[48:49]
	s_mov_b32 m0, s62
	s_nop 0
	global_load_lds_dwordx4 v150, s[48:49]
	s_waitcnt lgkmcnt(8)
	ds_read_b128 v[212:215], v163 offset:49152
	ds_read_b128 v[216:219], v163 offset:51200
	ds_read_b128 v[220:223], v164 offset:49152
	ds_read_b128 v[224:227], v164 offset:51200
	s_waitcnt vmcnt(8)
	s_waitcnt lgkmcnt(0)
	s_barrier
	s_waitcnt lgkmcnt(0)
	s_setprio 1
	s_waitcnt lgkmcnt(7)
	v_mfma_f32_16x16x128_f8f6f4 v[18:21], v[156:159], v[180:183], v[18:21] cbsz:4 blgp:4
	s_waitcnt lgkmcnt(5)
	v_mfma_f32_16x16x128_f8f6f4 v[18:21], v[172:175], v[188:191], v[18:21] cbsz:4 blgp:4
	v_mfma_f32_16x16x128_f8f6f4 v[22:25], v[168:171], v[180:183], v[22:25] cbsz:4 blgp:4
	s_nop 0
	v_mfma_f32_16x16x128_f8f6f4 v[22:25], v[176:179], v[188:191], v[22:25] cbsz:4 blgp:4
	v_mfma_f32_16x16x128_f8f6f4 v[26:29], v[156:159], v[184:187], v[26:29] cbsz:4 blgp:4
	s_waitcnt lgkmcnt(4)
	v_mfma_f32_16x16x128_f8f6f4 v[26:29], v[172:175], v[192:195], v[26:29] cbsz:4 blgp:4
	v_mfma_f32_16x16x128_f8f6f4 v[30:33], v[168:171], v[184:187], v[30:33] cbsz:4 blgp:4
	s_nop 0
	v_mfma_f32_16x16x128_f8f6f4 v[30:33], v[176:179], v[192:195], v[30:33] cbsz:4 blgp:4
	s_waitcnt lgkmcnt(3)
	v_mfma_f32_16x16x128_f8f6f4 v[34:37], v[156:159], v[196:199], v[34:37] cbsz:4 blgp:4
	s_waitcnt lgkmcnt(1)
	v_mfma_f32_16x16x128_f8f6f4 v[34:37], v[172:175], v[204:207], v[34:37] cbsz:4 blgp:4
	v_mfma_f32_16x16x128_f8f6f4 v[38:41], v[168:171], v[196:199], v[38:41] cbsz:4 blgp:4
	s_nop 0
	v_mfma_f32_16x16x128_f8f6f4 v[38:41], v[176:179], v[204:207], v[38:41] cbsz:4 blgp:4
	v_mfma_f32_16x16x128_f8f6f4 v[42:45], v[156:159], v[200:203], v[42:45] cbsz:4 blgp:4
	s_waitcnt lgkmcnt(0)
	v_mfma_f32_16x16x128_f8f6f4 v[42:45], v[172:175], v[208:211], v[42:45] cbsz:4 blgp:4
	v_mfma_f32_16x16x128_f8f6f4 v[46:49], v[168:171], v[200:203], v[46:49] cbsz:4 blgp:4
	s_nop 0
	v_mfma_f32_16x16x128_f8f6f4 v[46:49], v[176:179], v[208:211], v[46:49] cbsz:4 blgp:4
	s_waitcnt lgkmcnt(3)
	v_mfma_f32_16x16x128_f8f6f4 v[50:53], v[212:215], v[180:183], v[50:53] cbsz:4 blgp:4
	s_waitcnt lgkmcnt(1)
	v_mfma_f32_16x16x128_f8f6f4 v[50:53], v[220:223], v[188:191], v[50:53] cbsz:4 blgp:4
	v_mfma_f32_16x16x128_f8f6f4 v[54:57], v[216:219], v[180:183], v[54:57] cbsz:4 blgp:4
	s_waitcnt lgkmcnt(0)
	v_mfma_f32_16x16x128_f8f6f4 v[54:57], v[224:227], v[188:191], v[54:57] cbsz:4 blgp:4
	v_mfma_f32_16x16x128_f8f6f4 v[58:61], v[212:215], v[184:187], v[58:61] cbsz:4 blgp:4
	s_nop 0
	v_mfma_f32_16x16x128_f8f6f4 v[58:61], v[220:223], v[192:195], v[58:61] cbsz:4 blgp:4
	v_mfma_f32_16x16x128_f8f6f4 v[62:65], v[216:219], v[184:187], v[62:65] cbsz:4 blgp:4
	s_nop 0
	v_mfma_f32_16x16x128_f8f6f4 v[62:65], v[224:227], v[192:195], v[62:65] cbsz:4 blgp:4
	v_mfma_f32_16x16x128_f8f6f4 v[66:69], v[212:215], v[196:199], v[66:69] cbsz:4 blgp:4
	s_nop 0
	v_mfma_f32_16x16x128_f8f6f4 v[66:69], v[220:223], v[204:207], v[66:69] cbsz:4 blgp:4
	v_mfma_f32_16x16x128_f8f6f4 v[70:73], v[216:219], v[196:199], v[70:73] cbsz:4 blgp:4
	s_nop 0
	v_mfma_f32_16x16x128_f8f6f4 v[70:73], v[224:227], v[204:207], v[70:73] cbsz:4 blgp:4
	v_mfma_f32_16x16x128_f8f6f4 v[74:77], v[212:215], v[200:203], v[74:77] cbsz:4 blgp:4
	s_nop 0
	v_mfma_f32_16x16x128_f8f6f4 v[74:77], v[220:223], v[208:211], v[74:77] cbsz:4 blgp:4
	v_mfma_f32_16x16x128_f8f6f4 v[78:81], v[216:219], v[200:203], v[78:81] cbsz:4 blgp:4
	s_nop 0
	v_mfma_f32_16x16x128_f8f6f4 v[78:81], v[224:227], v[208:211], v[78:81] cbsz:4 blgp:4
	s_setprio 0
	s_barrier
	s_mov_b32 m0, s65
	s_nop 0
	global_load_lds_dwordx4 v148, s[44:45]
	s_mov_b32 m0, s66
	s_nop 0
	global_load_lds_dwordx4 v152, s[44:45]
	ds_read_b128 v[180:183], v165 offset:49152
	ds_read_b128 v[184:187], v165 offset:51200
	ds_read_b128 v[188:191], v166 offset:49152
	ds_read_b128 v[192:195], v166 offset:51200
	ds_read_b128 v[196:199], v165 offset:53248
	ds_read_b128 v[200:203], v165 offset:55296
	ds_read_b128 v[204:207], v166 offset:53248
	ds_read_b128 v[208:211], v166 offset:55296
	s_mov_b32 m0, s67
	s_nop 0
	global_load_lds_dwordx4 v146, s[46:47]
	s_mov_b32 m0, s68
	s_nop 0
	global_load_lds_dwordx4 v150, s[46:47]
	s_add_u32 s44, s44, s24
	s_addc_u32 s45, s45, s25
	s_mov_b32 m0, s69
	s_nop 0
	global_load_lds_dwordx4 v148, s[44:45]
	s_mov_b32 m0, s70
	s_nop 0
	global_load_lds_dwordx4 v152, s[44:45]
	s_waitcnt vmcnt(8)
	s_waitcnt lgkmcnt(0)
	s_barrier
	s_setprio 1
	s_waitcnt lgkmcnt(7)
	v_mfma_f32_16x16x128_f8f6f4 v[86:89], v[156:159], v[180:183], v[86:89] cbsz:4 blgp:4
	s_waitcnt lgkmcnt(5)
	v_mfma_f32_16x16x128_f8f6f4 v[86:89], v[172:175], v[188:191], v[86:89] cbsz:4 blgp:4
	v_mfma_f32_16x16x128_f8f6f4 v[90:93], v[168:171], v[180:183], v[90:93] cbsz:4 blgp:4
	s_nop 0
	v_mfma_f32_16x16x128_f8f6f4 v[90:93], v[176:179], v[188:191], v[90:93] cbsz:4 blgp:4
	v_mfma_f32_16x16x128_f8f6f4 v[98:101], v[156:159], v[184:187], v[98:101] cbsz:4 blgp:4
	s_waitcnt lgkmcnt(4)
	v_mfma_f32_16x16x128_f8f6f4 v[98:101], v[172:175], v[192:195], v[98:101] cbsz:4 blgp:4
	v_mfma_f32_16x16x128_f8f6f4 v[106:109], v[168:171], v[184:187], v[106:109] cbsz:4 blgp:4
	s_nop 0
	v_mfma_f32_16x16x128_f8f6f4 v[106:109], v[176:179], v[192:195], v[106:109] cbsz:4 blgp:4
	s_waitcnt lgkmcnt(3)
	v_mfma_f32_16x16x128_f8f6f4 v[118:121], v[156:159], v[196:199], v[118:121] cbsz:4 blgp:4
	s_waitcnt lgkmcnt(1)
	v_mfma_f32_16x16x128_f8f6f4 v[118:121], v[172:175], v[204:207], v[118:121] cbsz:4 blgp:4
	v_mfma_f32_16x16x128_f8f6f4 v[126:129], v[168:171], v[196:199], v[126:129] cbsz:4 blgp:4
	s_nop 0
	v_mfma_f32_16x16x128_f8f6f4 v[126:129], v[176:179], v[204:207], v[126:129] cbsz:4 blgp:4
	v_mfma_f32_16x16x128_f8f6f4 v[138:141], v[156:159], v[200:203], v[138:141] cbsz:4 blgp:4
	s_waitcnt lgkmcnt(0)
	v_mfma_f32_16x16x128_f8f6f4 v[138:141], v[172:175], v[208:211], v[138:141] cbsz:4 blgp:4
	v_mfma_f32_16x16x128_f8f6f4 v[82:85], v[168:171], v[200:203], v[82:85] cbsz:4 blgp:4
	s_nop 0
	v_mfma_f32_16x16x128_f8f6f4 v[82:85], v[176:179], v[208:211], v[82:85] cbsz:4 blgp:4
	v_mfma_f32_16x16x128_f8f6f4 v[94:97], v[212:215], v[180:183], v[94:97] cbsz:4 blgp:4
	s_nop 0
	v_mfma_f32_16x16x128_f8f6f4 v[94:97], v[220:223], v[188:191], v[94:97] cbsz:4 blgp:4
	v_mfma_f32_16x16x128_f8f6f4 v[102:105], v[216:219], v[180:183], v[102:105] cbsz:4 blgp:4
	s_nop 0
	v_mfma_f32_16x16x128_f8f6f4 v[102:105], v[224:227], v[188:191], v[102:105] cbsz:4 blgp:4
	v_mfma_f32_16x16x128_f8f6f4 v[110:113], v[212:215], v[184:187], v[110:113] cbsz:4 blgp:4
	s_nop 0
	v_mfma_f32_16x16x128_f8f6f4 v[110:113], v[220:223], v[192:195], v[110:113] cbsz:4 blgp:4
	v_mfma_f32_16x16x128_f8f6f4 v[114:117], v[216:219], v[184:187], v[114:117] cbsz:4 blgp:4
	s_nop 0
	v_mfma_f32_16x16x128_f8f6f4 v[114:117], v[224:227], v[192:195], v[114:117] cbsz:4 blgp:4
	v_mfma_f32_16x16x128_f8f6f4 v[122:125], v[212:215], v[196:199], v[122:125] cbsz:4 blgp:4
	s_nop 0
	v_mfma_f32_16x16x128_f8f6f4 v[122:125], v[220:223], v[204:207], v[122:125] cbsz:4 blgp:4
	v_mfma_f32_16x16x128_f8f6f4 v[130:133], v[216:219], v[196:199], v[130:133] cbsz:4 blgp:4
	s_nop 0
	v_mfma_f32_16x16x128_f8f6f4 v[130:133], v[224:227], v[204:207], v[130:133] cbsz:4 blgp:4
	v_mfma_f32_16x16x128_f8f6f4 v[134:137], v[212:215], v[200:203], v[134:137] cbsz:4 blgp:4
	s_nop 0
	v_mfma_f32_16x16x128_f8f6f4 v[134:137], v[220:223], v[208:211], v[134:137] cbsz:4 blgp:4
	v_mfma_f32_16x16x128_f8f6f4 v[142:145], v[216:219], v[200:203], v[142:145] cbsz:4 blgp:4
	s_nop 0
	v_mfma_f32_16x16x128_f8f6f4 v[142:145], v[224:227], v[208:211], v[142:145] cbsz:4 blgp:4
	s_setprio 0
	s_andn2_b64 vcc, exec, s[34:35]
	s_barrier
	s_cbranch_vccnz .LBB5_4
	s_ashr_i32 s29, s28, 31
	s_lshl_b64 s[44:45], s[28:29], 10
	s_add_u32 s44, s10, s44
	s_addc_u32 s45, s11, s45
	s_add_u32 s29, s42, 0x200
	s_addc_u32 s79, s43, 0
	s_add_u32 s80, s40, 0x200
	s_addc_u32 s81, s41, 0
	s_add_u32 s40, s82, 0x180
	s_addc_u32 s41, s83, 0
	s_mov_b32 s82, 4
	s_cmp_eq_u32 s64, s82
	s_cselect_b64 s[42:43], -1, 0
	s_cmp_lg_u32 s64, s82
	s_cbranch_scc1 .LBB5_15

.LBB5_15:
	ds_read_b128 v[156:159], v163
	ds_read_b128 v[168:171], v163 offset:2048
	ds_read_b128 v[172:175], v164
	ds_read_b128 v[176:179], v164 offset:2048
	s_and_b64 s[42:43], s[42:43], exec
	s_cselect_b32 s48, s38, s29
	s_cselect_b32 s49, s39, s79
	s_cselect_b32 s51, s5, s81
	s_cselect_b32 s50, s4, s80
	s_add_u32 s46, s48, 0x80
	s_addc_u32 s47, s49, 0
	s_add_u32 s42, s50, 0x80
	s_addc_u32 s43, s51, 0
	ds_read_b128 v[180:183], v165
	ds_read_b128 v[184:187], v165 offset:2048
	ds_read_b128 v[188:191], v166
	ds_read_b128 v[192:195], v166 offset:2048
	ds_read_b128 v[196:199], v165 offset:4096
	ds_read_b128 v[200:203], v165 offset:6144
	ds_read_b128 v[204:207], v166 offset:4096
	ds_read_b128 v[208:211], v166 offset:6144
	s_mov_b32 m0, s71
	s_nop 0
	global_load_lds_dwordx4 v146, s[40:41]
	s_mov_b32 m0, s72
	s_nop 0
	global_load_lds_dwordx4 v150, s[40:41]
	s_waitcnt lgkmcnt(8)
	ds_read_b128 v[212:215], v163 offset:16384
	ds_read_b128 v[216:219], v163 offset:18432
	ds_read_b128 v[220:223], v164 offset:16384
	ds_read_b128 v[224:227], v164 offset:18432
	s_waitcnt vmcnt(8)
	s_waitcnt lgkmcnt(0)
	s_barrier
	s_waitcnt lgkmcnt(0)
	s_setprio 1
	s_waitcnt lgkmcnt(7)
	v_mfma_f32_16x16x128_f8f6f4 v[18:21], v[156:159], v[180:183], v[18:21] cbsz:4 blgp:4
	s_waitcnt lgkmcnt(5)
	v_mfma_f32_16x16x128_f8f6f4 v[18:21], v[172:175], v[188:191], v[18:21] cbsz:4 blgp:4
	v_mfma_f32_16x16x128_f8f6f4 v[22:25], v[168:171], v[180:183], v[22:25] cbsz:4 blgp:4
	s_nop 0
	v_mfma_f32_16x16x128_f8f6f4 v[22:25], v[176:179], v[188:191], v[22:25] cbsz:4 blgp:4
	v_mfma_f32_16x16x128_f8f6f4 v[26:29], v[156:159], v[184:187], v[26:29] cbsz:4 blgp:4
	s_waitcnt lgkmcnt(4)
	v_mfma_f32_16x16x128_f8f6f4 v[26:29], v[172:175], v[192:195], v[26:29] cbsz:4 blgp:4
	v_mfma_f32_16x16x128_f8f6f4 v[30:33], v[168:171], v[184:187], v[30:33] cbsz:4 blgp:4
	s_nop 0
	v_mfma_f32_16x16x128_f8f6f4 v[30:33], v[176:179], v[192:195], v[30:33] cbsz:4 blgp:4
	s_waitcnt lgkmcnt(3)
	v_mfma_f32_16x16x128_f8f6f4 v[34:37], v[156:159], v[196:199], v[34:37] cbsz:4 blgp:4
	s_waitcnt lgkmcnt(1)
	v_mfma_f32_16x16x128_f8f6f4 v[34:37], v[172:175], v[204:207], v[34:37] cbsz:4 blgp:4
	v_mfma_f32_16x16x128_f8f6f4 v[38:41], v[168:171], v[196:199], v[38:41] cbsz:4 blgp:4
	s_nop 0
	v_mfma_f32_16x16x128_f8f6f4 v[38:41], v[176:179], v[204:207], v[38:41] cbsz:4 blgp:4
	v_mfma_f32_16x16x128_f8f6f4 v[42:45], v[156:159], v[200:203], v[42:45] cbsz:4 blgp:4
	s_waitcnt lgkmcnt(0)
	v_mfma_f32_16x16x128_f8f6f4 v[42:45], v[172:175], v[208:211], v[42:45] cbsz:4 blgp:4
	v_mfma_f32_16x16x128_f8f6f4 v[46:49], v[168:171], v[200:203], v[46:49] cbsz:4 blgp:4
	s_nop 0
	v_mfma_f32_16x16x128_f8f6f4 v[46:49], v[176:179], v[208:211], v[46:49] cbsz:4 blgp:4
	s_waitcnt lgkmcnt(3)
	v_mfma_f32_16x16x128_f8f6f4 v[50:53], v[212:215], v[180:183], v[50:53] cbsz:4 blgp:4
	s_waitcnt lgkmcnt(1)
	v_mfma_f32_16x16x128_f8f6f4 v[50:53], v[220:223], v[188:191], v[50:53] cbsz:4 blgp:4
	v_mfma_f32_16x16x128_f8f6f4 v[54:57], v[216:219], v[180:183], v[54:57] cbsz:4 blgp:4
	s_waitcnt lgkmcnt(0)
	v_mfma_f32_16x16x128_f8f6f4 v[54:57], v[224:227], v[188:191], v[54:57] cbsz:4 blgp:4
	v_mfma_f32_16x16x128_f8f6f4 v[58:61], v[212:215], v[184:187], v[58:61] cbsz:4 blgp:4
	s_nop 0
	v_mfma_f32_16x16x128_f8f6f4 v[58:61], v[220:223], v[192:195], v[58:61] cbsz:4 blgp:4
	v_mfma_f32_16x16x128_f8f6f4 v[62:65], v[216:219], v[184:187], v[62:65] cbsz:4 blgp:4
	s_nop 0
	v_mfma_f32_16x16x128_f8f6f4 v[62:65], v[224:227], v[192:195], v[62:65] cbsz:4 blgp:4
	v_mfma_f32_16x16x128_f8f6f4 v[66:69], v[212:215], v[196:199], v[66:69] cbsz:4 blgp:4
	s_nop 0
	v_mfma_f32_16x16x128_f8f6f4 v[66:69], v[220:223], v[204:207], v[66:69] cbsz:4 blgp:4
	v_mfma_f32_16x16x128_f8f6f4 v[70:73], v[216:219], v[196:199], v[70:73] cbsz:4 blgp:4
	s_nop 0
	v_mfma_f32_16x16x128_f8f6f4 v[70:73], v[224:227], v[204:207], v[70:73] cbsz:4 blgp:4
	v_mfma_f32_16x16x128_f8f6f4 v[74:77], v[212:215], v[200:203], v[74:77] cbsz:4 blgp:4
	s_nop 0
	v_mfma_f32_16x16x128_f8f6f4 v[74:77], v[220:223], v[208:211], v[74:77] cbsz:4 blgp:4
	v_mfma_f32_16x16x128_f8f6f4 v[78:81], v[216:219], v[200:203], v[78:81] cbsz:4 blgp:4
	s_nop 0
	v_mfma_f32_16x16x128_f8f6f4 v[78:81], v[224:227], v[208:211], v[78:81] cbsz:4 blgp:4
	s_setprio 0
	s_barrier
	s_mov_b32 m0, s56
	s_nop 0
	global_load_lds_dwordx4 v148, s[50:51]
	s_mov_b32 m0, s57
	s_nop 0
	global_load_lds_dwordx4 v152, s[50:51]
	ds_read_b128 v[180:183], v165 offset:16384
	ds_read_b128 v[184:187], v165 offset:18432
	ds_read_b128 v[188:191], v166 offset:16384
	ds_read_b128 v[192:195], v166 offset:18432
	ds_read_b128 v[196:199], v165 offset:20480
	ds_read_b128 v[200:203], v165 offset:22528
	ds_read_b128 v[204:207], v166 offset:20480
	ds_read_b128 v[208:211], v166 offset:22528
	s_mov_b32 m0, s55
	s_nop 0
	global_load_lds_dwordx4 v146, s[48:49]
	s_mov_b32 m0, s58
	s_nop 0
	global_load_lds_dwordx4 v150, s[48:49]
	s_add_u32 s50, s50, s24
	s_addc_u32 s51, s51, s25
	s_mov_b32 m0, s59
	s_nop 0
	global_load_lds_dwordx4 v148, s[50:51]
	s_mov_b32 m0, s60
	s_nop 0
	global_load_lds_dwordx4 v152, s[50:51]
	s_waitcnt vmcnt(8)
	s_waitcnt lgkmcnt(0)
	s_barrier
	s_setprio 1
	s_waitcnt lgkmcnt(7)
	v_mfma_f32_16x16x128_f8f6f4 v[86:89], v[156:159], v[180:183], v[86:89] cbsz:4 blgp:4
	s_waitcnt lgkmcnt(5)
	v_mfma_f32_16x16x128_f8f6f4 v[86:89], v[172:175], v[188:191], v[86:89] cbsz:4 blgp:4
	v_mfma_f32_16x16x128_f8f6f4 v[90:93], v[168:171], v[180:183], v[90:93] cbsz:4 blgp:4
	s_nop 0
	v_mfma_f32_16x16x128_f8f6f4 v[90:93], v[176:179], v[188:191], v[90:93] cbsz:4 blgp:4
	v_mfma_f32_16x16x128_f8f6f4 v[98:101], v[156:159], v[184:187], v[98:101] cbsz:4 blgp:4
	s_waitcnt lgkmcnt(4)
	v_mfma_f32_16x16x128_f8f6f4 v[98:101], v[172:175], v[192:195], v[98:101] cbsz:4 blgp:4
	v_mfma_f32_16x16x128_f8f6f4 v[106:109], v[168:171], v[184:187], v[106:109] cbsz:4 blgp:4
	s_nop 0
	v_mfma_f32_16x16x128_f8f6f4 v[106:109], v[176:179], v[192:195], v[106:109] cbsz:4 blgp:4
	s_waitcnt lgkmcnt(3)
	v_mfma_f32_16x16x128_f8f6f4 v[118:121], v[156:159], v[196:199], v[118:121] cbsz:4 blgp:4
	s_waitcnt lgkmcnt(1)
	v_mfma_f32_16x16x128_f8f6f4 v[118:121], v[172:175], v[204:207], v[118:121] cbsz:4 blgp:4
	v_mfma_f32_16x16x128_f8f6f4 v[126:129], v[168:171], v[196:199], v[126:129] cbsz:4 blgp:4
	s_nop 0
	v_mfma_f32_16x16x128_f8f6f4 v[126:129], v[176:179], v[204:207], v[126:129] cbsz:4 blgp:4
	v_mfma_f32_16x16x128_f8f6f4 v[138:141], v[156:159], v[200:203], v[138:141] cbsz:4 blgp:4
	s_waitcnt lgkmcnt(0)
	v_mfma_f32_16x16x128_f8f6f4 v[138:141], v[172:175], v[208:211], v[138:141] cbsz:4 blgp:4
	v_mfma_f32_16x16x128_f8f6f4 v[82:85], v[168:171], v[200:203], v[82:85] cbsz:4 blgp:4
	s_nop 0
	v_mfma_f32_16x16x128_f8f6f4 v[82:85], v[176:179], v[208:211], v[82:85] cbsz:4 blgp:4
	v_mfma_f32_16x16x128_f8f6f4 v[94:97], v[212:215], v[180:183], v[94:97] cbsz:4 blgp:4
	s_nop 0
	v_mfma_f32_16x16x128_f8f6f4 v[94:97], v[220:223], v[188:191], v[94:97] cbsz:4 blgp:4
	v_mfma_f32_16x16x128_f8f6f4 v[102:105], v[216:219], v[180:183], v[102:105] cbsz:4 blgp:4
	s_nop 0
	v_mfma_f32_16x16x128_f8f6f4 v[102:105], v[224:227], v[188:191], v[102:105] cbsz:4 blgp:4
	v_mfma_f32_16x16x128_f8f6f4 v[110:113], v[212:215], v[184:187], v[110:113] cbsz:4 blgp:4
	s_nop 0
	v_mfma_f32_16x16x128_f8f6f4 v[110:113], v[220:223], v[192:195], v[110:113] cbsz:4 blgp:4
	v_mfma_f32_16x16x128_f8f6f4 v[114:117], v[216:219], v[184:187], v[114:117] cbsz:4 blgp:4
	s_nop 0
	v_mfma_f32_16x16x128_f8f6f4 v[114:117], v[224:227], v[192:195], v[114:117] cbsz:4 blgp:4
	v_mfma_f32_16x16x128_f8f6f4 v[122:125], v[212:215], v[196:199], v[122:125] cbsz:4 blgp:4
	s_nop 0
	v_mfma_f32_16x16x128_f8f6f4 v[122:125], v[220:223], v[204:207], v[122:125] cbsz:4 blgp:4
	v_mfma_f32_16x16x128_f8f6f4 v[130:133], v[216:219], v[196:199], v[130:133] cbsz:4 blgp:4
	s_nop 0
	v_mfma_f32_16x16x128_f8f6f4 v[130:133], v[224:227], v[204:207], v[130:133] cbsz:4 blgp:4
	v_mfma_f32_16x16x128_f8f6f4 v[134:137], v[212:215], v[200:203], v[134:137] cbsz:4 blgp:4
	s_nop 0
	v_mfma_f32_16x16x128_f8f6f4 v[134:137], v[220:223], v[208:211], v[134:137] cbsz:4 blgp:4
	v_mfma_f32_16x16x128_f8f6f4 v[142:145], v[216:219], v[200:203], v[142:145] cbsz:4 blgp:4
	s_nop 0
	v_mfma_f32_16x16x128_f8f6f4 v[142:145], v[224:227], v[208:211], v[142:145] cbsz:4 blgp:4
	s_setprio 0
	s_barrier
	ds_read_b128 v[156:159], v163 offset:32768
	ds_read_b128 v[168:171], v163 offset:34816
	ds_read_b128 v[172:175], v164 offset:32768
	ds_read_b128 v[176:179], v164 offset:34816
	ds_read_b128 v[180:183], v165 offset:32768
	ds_read_b128 v[184:187], v165 offset:34816
	ds_read_b128 v[188:191], v166 offset:32768
	ds_read_b128 v[192:195], v166 offset:34816
	ds_read_b128 v[196:199], v165 offset:36864
	ds_read_b128 v[200:203], v165 offset:38912
	ds_read_b128 v[204:207], v166 offset:36864
	ds_read_b128 v[208:211], v166 offset:38912
	s_add_u32 s48, s48, s22
	s_addc_u32 s49, s49, s23
	s_mov_b32 m0, s61
	s_nop 0
	global_load_lds_dwordx4 v146, s[48:49]
	s_mov_b32 m0, s62
	s_nop 0
	global_load_lds_dwordx4 v150, s[48:49]
	s_waitcnt lgkmcnt(8)
	ds_read_b128 v[212:215], v163 offset:49152
	ds_read_b128 v[216:219], v163 offset:51200
	ds_read_b128 v[220:223], v164 offset:49152
	ds_read_b128 v[224:227], v164 offset:51200
	s_waitcnt vmcnt(8)
	s_waitcnt lgkmcnt(0)
	s_barrier
	s_waitcnt lgkmcnt(0)
	s_setprio 1
	s_waitcnt lgkmcnt(7)
	v_mfma_f32_16x16x128_f8f6f4 v[18:21], v[156:159], v[180:183], v[18:21] cbsz:4 blgp:4
	s_waitcnt lgkmcnt(5)
	v_mfma_f32_16x16x128_f8f6f4 v[18:21], v[172:175], v[188:191], v[18:21] cbsz:4 blgp:4
	v_mfma_f32_16x16x128_f8f6f4 v[22:25], v[168:171], v[180:183], v[22:25] cbsz:4 blgp:4
	s_nop 0
	v_mfma_f32_16x16x128_f8f6f4 v[22:25], v[176:179], v[188:191], v[22:25] cbsz:4 blgp:4
	v_mfma_f32_16x16x128_f8f6f4 v[26:29], v[156:159], v[184:187], v[26:29] cbsz:4 blgp:4
	s_waitcnt lgkmcnt(4)
	v_mfma_f32_16x16x128_f8f6f4 v[26:29], v[172:175], v[192:195], v[26:29] cbsz:4 blgp:4
	v_mfma_f32_16x16x128_f8f6f4 v[30:33], v[168:171], v[184:187], v[30:33] cbsz:4 blgp:4
	s_nop 0
	v_mfma_f32_16x16x128_f8f6f4 v[30:33], v[176:179], v[192:195], v[30:33] cbsz:4 blgp:4
	s_waitcnt lgkmcnt(3)
	v_mfma_f32_16x16x128_f8f6f4 v[34:37], v[156:159], v[196:199], v[34:37] cbsz:4 blgp:4
	s_waitcnt lgkmcnt(1)
	v_mfma_f32_16x16x128_f8f6f4 v[34:37], v[172:175], v[204:207], v[34:37] cbsz:4 blgp:4
	v_mfma_f32_16x16x128_f8f6f4 v[38:41], v[168:171], v[196:199], v[38:41] cbsz:4 blgp:4
	s_nop 0
	v_mfma_f32_16x16x128_f8f6f4 v[38:41], v[176:179], v[204:207], v[38:41] cbsz:4 blgp:4
	v_mfma_f32_16x16x128_f8f6f4 v[42:45], v[156:159], v[200:203], v[42:45] cbsz:4 blgp:4
	s_waitcnt lgkmcnt(0)
	v_mfma_f32_16x16x128_f8f6f4 v[42:45], v[172:175], v[208:211], v[42:45] cbsz:4 blgp:4
	v_mfma_f32_16x16x128_f8f6f4 v[46:49], v[168:171], v[200:203], v[46:49] cbsz:4 blgp:4
	s_nop 0
	v_mfma_f32_16x16x128_f8f6f4 v[46:49], v[176:179], v[208:211], v[46:49] cbsz:4 blgp:4
	s_waitcnt lgkmcnt(3)
	v_mfma_f32_16x16x128_f8f6f4 v[50:53], v[212:215], v[180:183], v[50:53] cbsz:4 blgp:4
	s_waitcnt lgkmcnt(1)
	v_mfma_f32_16x16x128_f8f6f4 v[50:53], v[220:223], v[188:191], v[50:53] cbsz:4 blgp:4
	v_mfma_f32_16x16x128_f8f6f4 v[54:57], v[216:219], v[180:183], v[54:57] cbsz:4 blgp:4
	s_waitcnt lgkmcnt(0)
	v_mfma_f32_16x16x128_f8f6f4 v[54:57], v[224:227], v[188:191], v[54:57] cbsz:4 blgp:4
	v_mfma_f32_16x16x128_f8f6f4 v[58:61], v[212:215], v[184:187], v[58:61] cbsz:4 blgp:4
	s_nop 0
	v_mfma_f32_16x16x128_f8f6f4 v[58:61], v[220:223], v[192:195], v[58:61] cbsz:4 blgp:4
	v_mfma_f32_16x16x128_f8f6f4 v[62:65], v[216:219], v[184:187], v[62:65] cbsz:4 blgp:4
	s_nop 0
	v_mfma_f32_16x16x128_f8f6f4 v[62:65], v[224:227], v[192:195], v[62:65] cbsz:4 blgp:4
	v_mfma_f32_16x16x128_f8f6f4 v[66:69], v[212:215], v[196:199], v[66:69] cbsz:4 blgp:4
	s_nop 0
	v_mfma_f32_16x16x128_f8f6f4 v[66:69], v[220:223], v[204:207], v[66:69] cbsz:4 blgp:4
	v_mfma_f32_16x16x128_f8f6f4 v[70:73], v[216:219], v[196:199], v[70:73] cbsz:4 blgp:4
	s_nop 0
	v_mfma_f32_16x16x128_f8f6f4 v[70:73], v[224:227], v[204:207], v[70:73] cbsz:4 blgp:4
	v_mfma_f32_16x16x128_f8f6f4 v[74:77], v[212:215], v[200:203], v[74:77] cbsz:4 blgp:4
	s_nop 0
	v_mfma_f32_16x16x128_f8f6f4 v[74:77], v[220:223], v[208:211], v[74:77] cbsz:4 blgp:4
	v_mfma_f32_16x16x128_f8f6f4 v[78:81], v[216:219], v[200:203], v[78:81] cbsz:4 blgp:4
	s_nop 0
	v_mfma_f32_16x16x128_f8f6f4 v[78:81], v[224:227], v[208:211], v[78:81] cbsz:4 blgp:4
	s_setprio 0
	s_barrier
	s_mov_b32 m0, s65
	s_nop 0
	global_load_lds_dwordx4 v148, s[42:43]
	s_mov_b32 m0, s66
	s_nop 0
	global_load_lds_dwordx4 v152, s[42:43]
	ds_read_b128 v[180:183], v165 offset:49152
	ds_read_b128 v[184:187], v165 offset:51200
	ds_read_b128 v[188:191], v166 offset:49152
	ds_read_b128 v[192:195], v166 offset:51200
	ds_read_b128 v[196:199], v165 offset:53248
	ds_read_b128 v[200:203], v165 offset:55296
	ds_read_b128 v[204:207], v166 offset:53248
	ds_read_b128 v[208:211], v166 offset:55296
	s_mov_b32 m0, s67
	s_nop 0
	global_load_lds_dwordx4 v146, s[46:47]
	s_mov_b32 m0, s68
	s_nop 0
	global_load_lds_dwordx4 v150, s[46:47]
	s_add_u32 s42, s42, s24
	s_addc_u32 s43, s43, s25
	s_mov_b32 m0, s69
	s_nop 0
	global_load_lds_dwordx4 v148, s[42:43]
	s_mov_b32 m0, s70
	s_nop 0
	global_load_lds_dwordx4 v152, s[42:43]
	s_waitcnt vmcnt(8)
	s_waitcnt lgkmcnt(0)
	s_barrier
	s_setprio 1
	s_waitcnt lgkmcnt(7)
	v_mfma_f32_16x16x128_f8f6f4 v[86:89], v[156:159], v[180:183], v[86:89] cbsz:4 blgp:4
	s_waitcnt lgkmcnt(5)
	v_mfma_f32_16x16x128_f8f6f4 v[86:89], v[172:175], v[188:191], v[86:89] cbsz:4 blgp:4
	v_mfma_f32_16x16x128_f8f6f4 v[90:93], v[168:171], v[180:183], v[90:93] cbsz:4 blgp:4
	s_nop 0
	v_mfma_f32_16x16x128_f8f6f4 v[90:93], v[176:179], v[188:191], v[90:93] cbsz:4 blgp:4
	v_mfma_f32_16x16x128_f8f6f4 v[98:101], v[156:159], v[184:187], v[98:101] cbsz:4 blgp:4
	s_waitcnt lgkmcnt(4)
	v_mfma_f32_16x16x128_f8f6f4 v[98:101], v[172:175], v[192:195], v[98:101] cbsz:4 blgp:4
	v_mfma_f32_16x16x128_f8f6f4 v[106:109], v[168:171], v[184:187], v[106:109] cbsz:4 blgp:4
	s_nop 0
	v_mfma_f32_16x16x128_f8f6f4 v[106:109], v[176:179], v[192:195], v[106:109] cbsz:4 blgp:4
	s_waitcnt lgkmcnt(3)
	v_mfma_f32_16x16x128_f8f6f4 v[118:121], v[156:159], v[196:199], v[118:121] cbsz:4 blgp:4
	s_waitcnt lgkmcnt(1)
	v_mfma_f32_16x16x128_f8f6f4 v[118:121], v[172:175], v[204:207], v[118:121] cbsz:4 blgp:4
	v_mfma_f32_16x16x128_f8f6f4 v[126:129], v[168:171], v[196:199], v[126:129] cbsz:4 blgp:4
	s_nop 0
	v_mfma_f32_16x16x128_f8f6f4 v[126:129], v[176:179], v[204:207], v[126:129] cbsz:4 blgp:4
	v_mfma_f32_16x16x128_f8f6f4 v[138:141], v[156:159], v[200:203], v[138:141] cbsz:4 blgp:4
	s_waitcnt lgkmcnt(0)
	v_mfma_f32_16x16x128_f8f6f4 v[138:141], v[172:175], v[208:211], v[138:141] cbsz:4 blgp:4
	v_mfma_f32_16x16x128_f8f6f4 v[82:85], v[168:171], v[200:203], v[82:85] cbsz:4 blgp:4
	s_nop 0
	v_mfma_f32_16x16x128_f8f6f4 v[82:85], v[176:179], v[208:211], v[82:85] cbsz:4 blgp:4
	v_mfma_f32_16x16x128_f8f6f4 v[94:97], v[212:215], v[180:183], v[94:97] cbsz:4 blgp:4
	s_nop 0
	v_mfma_f32_16x16x128_f8f6f4 v[94:97], v[220:223], v[188:191], v[94:97] cbsz:4 blgp:4
	v_mfma_f32_16x16x128_f8f6f4 v[102:105], v[216:219], v[180:183], v[102:105] cbsz:4 blgp:4
	s_nop 0
	v_mfma_f32_16x16x128_f8f6f4 v[102:105], v[224:227], v[188:191], v[102:105] cbsz:4 blgp:4
	v_mfma_f32_16x16x128_f8f6f4 v[110:113], v[212:215], v[184:187], v[110:113] cbsz:4 blgp:4
	s_nop 0
	v_mfma_f32_16x16x128_f8f6f4 v[110:113], v[220:223], v[192:195], v[110:113] cbsz:4 blgp:4
	v_mfma_f32_16x16x128_f8f6f4 v[114:117], v[216:219], v[184:187], v[114:117] cbsz:4 blgp:4
	s_nop 0
	v_mfma_f32_16x16x128_f8f6f4 v[114:117], v[224:227], v[192:195], v[114:117] cbsz:4 blgp:4
	v_mfma_f32_16x16x128_f8f6f4 v[122:125], v[212:215], v[196:199], v[122:125] cbsz:4 blgp:4
	s_nop 0
	v_mfma_f32_16x16x128_f8f6f4 v[122:125], v[220:223], v[204:207], v[122:125] cbsz:4 blgp:4
	v_mfma_f32_16x16x128_f8f6f4 v[130:133], v[216:219], v[196:199], v[130:133] cbsz:4 blgp:4
	s_nop 0
	v_mfma_f32_16x16x128_f8f6f4 v[130:133], v[224:227], v[204:207], v[130:133] cbsz:4 blgp:4
	v_mfma_f32_16x16x128_f8f6f4 v[134:137], v[212:215], v[200:203], v[134:137] cbsz:4 blgp:4
	s_nop 0
	v_mfma_f32_16x16x128_f8f6f4 v[134:137], v[220:223], v[208:211], v[134:137] cbsz:4 blgp:4
	v_mfma_f32_16x16x128_f8f6f4 v[142:145], v[216:219], v[200:203], v[142:145] cbsz:4 blgp:4
	s_nop 0
	v_mfma_f32_16x16x128_f8f6f4 v[142:145], v[224:227], v[208:211], v[142:145] cbsz:4 blgp:4
	s_setprio 0
	s_add_i32 s42, s82, 2
	s_add_u32 s29, s29, 0x100
	s_addc_u32 s79, s79, 0
	s_add_u32 s80, s80, 0x100
	s_addc_u32 s81, s81, 0
	s_add_u32 s40, s40, 0x100
	s_addc_u32 s41, s41, 0
	s_cmp_ge_i32 s82, s64
	s_barrier
	s_cbranch_scc1 .LBB5_4
	s_mov_b32 s82, s42
	s_cmp_eq_u32 s64, s82
	s_cselect_b64 s[42:43], -1, 0
	s_cmp_lg_u32 s64, s82
	s_cbranch_scc0 .LBB5_14
	s_branch .LBB5_15

.LBB6_15:
	s_add_u32 s82, s36, s20
	s_addc_u32 s83, s37, s21
	s_add_u32 s31, s36, 0x100
	s_addc_u32 s39, s37, 0
	s_and_b64 s[40:41], s[12:13], exec
	ds_read_b128 v[82:85], v169
	ds_read_b128 v[94:97], v169 offset:2048
	ds_read_b128 v[102:105], v178
	ds_read_b128 v[110:113], v178 offset:2048
	s_cselect_b32 s45, s5, s39
	s_cselect_b32 s44, s4, s31
	s_add_u32 s31, s34, 0x100
	s_addc_u32 s39, s35, 0
	s_and_b64 s[40:41], s[12:13], exec
	s_cselect_b32 s47, s7, s39
	s_cselect_b32 s46, s6, s31
	s_add_u32 s42, s44, 0x80
	s_addc_u32 s43, s45, 0
	s_add_u32 s40, s46, 0x80
	s_addc_u32 s41, s47, 0
	ds_read_b128 v[58:61], v179
	ds_read_b128 v[66:69], v179 offset:2048
	ds_read_b128 v[62:65], v180
	ds_read_b128 v[70:73], v180 offset:2048
	ds_read_b128 v[74:77], v179 offset:4096
	ds_read_b128 v[86:89], v179 offset:6144
	ds_read_b128 v[78:81], v180 offset:4096
	ds_read_b128 v[90:93], v180 offset:6144
	s_add_u32 s84, s82, 0x80
	s_addc_u32 s85, s83, 0
	s_mov_b32 m0, s68
	s_nop 0
	global_load_lds_dwordx4 v162, s[84:85]
	s_mov_b32 m0, s69
	s_nop 0
	global_load_lds_dwordx4 v166, s[84:85]
	s_waitcnt lgkmcnt(8)
	ds_read_b128 v[142:145], v169 offset:16384
	ds_read_b128 v[146:149], v169 offset:18432
	ds_read_b128 v[150:153], v178 offset:16384
	ds_read_b128 v[154:157], v178 offset:18432
	s_waitcnt vmcnt(8)
	s_waitcnt lgkmcnt(0)
	s_barrier
	s_waitcnt lgkmcnt(0)
	s_waitcnt vmcnt(16)
	v_mov_b32_e32 v171, v170
	v_pk_mul_f32 v[16:17], v[170:171], v[16:17]
	v_pk_mul_f32 v[14:15], v[172:173], v[14:15]
	v_pk_mul_f32 v[12:13], v[170:171], v[12:13]
	v_pk_mul_f32 v[10:11], v[172:173], v[10:11]
	v_pk_mul_f32 v[8:9], v[170:171], v[8:9]
	v_pk_mul_f32 v[6:7], v[172:173], v[6:7]
	v_pk_mul_f32 v[4:5], v[170:171], v[4:5]
	v_pk_mul_f32 v[2:3], v[172:173], v[2:3]
	s_setprio 1
	s_waitcnt lgkmcnt(7)
	v_mfma_f32_16x16x128_f8f6f4 v[18:21], v[82:85], v[58:61], v[14:17] cbsz:4 blgp:4
	s_waitcnt lgkmcnt(5)
	v_mfma_f32_16x16x128_f8f6f4 v[18:21], v[102:105], v[62:65], v[18:21] cbsz:4 blgp:4
	v_mfma_f32_16x16x128_f8f6f4 v[22:25], v[94:97], v[58:61], v[10:13] cbsz:4 blgp:4
	s_nop 0
	v_mfma_f32_16x16x128_f8f6f4 v[22:25], v[110:113], v[62:65], v[22:25] cbsz:4 blgp:4
	v_mfma_f32_16x16x128_f8f6f4 v[26:29], v[82:85], v[66:69], v[14:17] cbsz:4 blgp:4
	s_waitcnt lgkmcnt(4)
	v_mfma_f32_16x16x128_f8f6f4 v[26:29], v[102:105], v[70:73], v[26:29] cbsz:4 blgp:4
	v_mfma_f32_16x16x128_f8f6f4 v[30:33], v[94:97], v[66:69], v[10:13] cbsz:4 blgp:4
	s_nop 0
	v_mfma_f32_16x16x128_f8f6f4 v[30:33], v[110:113], v[70:73], v[30:33] cbsz:4 blgp:4
	s_waitcnt lgkmcnt(3)
	v_mfma_f32_16x16x128_f8f6f4 v[34:37], v[82:85], v[74:77], v[14:17] cbsz:4 blgp:4
	s_waitcnt lgkmcnt(1)
	v_mfma_f32_16x16x128_f8f6f4 v[34:37], v[102:105], v[78:81], v[34:37] cbsz:4 blgp:4
	v_mfma_f32_16x16x128_f8f6f4 v[38:41], v[94:97], v[74:77], v[10:13] cbsz:4 blgp:4
	s_nop 0
	v_mfma_f32_16x16x128_f8f6f4 v[38:41], v[110:113], v[78:81], v[38:41] cbsz:4 blgp:4
	v_mfma_f32_16x16x128_f8f6f4 v[42:45], v[82:85], v[86:89], v[14:17] cbsz:4 blgp:4
	s_waitcnt lgkmcnt(0)
	v_mfma_f32_16x16x128_f8f6f4 v[42:45], v[102:105], v[90:93], v[42:45] cbsz:4 blgp:4
	v_mfma_f32_16x16x128_f8f6f4 v[46:49], v[94:97], v[86:89], v[10:13] cbsz:4 blgp:4
	s_nop 0
	v_mfma_f32_16x16x128_f8f6f4 v[46:49], v[110:113], v[90:93], v[46:49] cbsz:4 blgp:4
	s_waitcnt lgkmcnt(3)
	v_mfma_f32_16x16x128_f8f6f4 v[50:53], v[142:145], v[58:61], v[6:9] cbsz:4 blgp:4
	s_waitcnt lgkmcnt(1)
	v_mfma_f32_16x16x128_f8f6f4 v[50:53], v[150:153], v[62:65], v[50:53] cbsz:4 blgp:4
	v_mfma_f32_16x16x128_f8f6f4 v[54:57], v[146:149], v[58:61], v[2:5] cbsz:4 blgp:4
	s_waitcnt lgkmcnt(0)
	v_mfma_f32_16x16x128_f8f6f4 v[54:57], v[154:157], v[62:65], v[54:57] cbsz:4 blgp:4
	v_mfma_f32_16x16x128_f8f6f4 v[58:61], v[142:145], v[66:69], v[6:9] cbsz:4 blgp:4
	s_nop 0
	v_mfma_f32_16x16x128_f8f6f4 v[58:61], v[150:153], v[70:73], v[58:61] cbsz:4 blgp:4
	v_mfma_f32_16x16x128_f8f6f4 v[62:65], v[146:149], v[66:69], v[2:5] cbsz:4 blgp:4
	s_nop 0
	v_mfma_f32_16x16x128_f8f6f4 v[62:65], v[154:157], v[70:73], v[62:65] cbsz:4 blgp:4
	v_mfma_f32_16x16x128_f8f6f4 v[66:69], v[142:145], v[74:77], v[6:9] cbsz:4 blgp:4
	s_nop 0
	v_mfma_f32_16x16x128_f8f6f4 v[66:69], v[150:153], v[78:81], v[66:69] cbsz:4 blgp:4
	v_mfma_f32_16x16x128_f8f6f4 v[70:73], v[146:149], v[74:77], v[2:5] cbsz:4 blgp:4
	s_nop 0
	v_mfma_f32_16x16x128_f8f6f4 v[70:73], v[154:157], v[78:81], v[70:73] cbsz:4 blgp:4
	v_mfma_f32_16x16x128_f8f6f4 v[74:77], v[142:145], v[86:89], v[6:9] cbsz:4 blgp:4
	s_nop 0
	v_mfma_f32_16x16x128_f8f6f4 v[74:77], v[150:153], v[90:93], v[74:77] cbsz:4 blgp:4
	v_mfma_f32_16x16x128_f8f6f4 v[78:81], v[146:149], v[86:89], v[2:5] cbsz:4 blgp:4
	s_nop 0
	v_mfma_f32_16x16x128_f8f6f4 v[78:81], v[154:157], v[90:93], v[78:81] cbsz:4 blgp:4
	s_setprio 0
	s_barrier
	s_mov_b32 m0, s54
	s_nop 0
	global_load_lds_dwordx4 v164, s[46:47]
	s_mov_b32 m0, s55
	s_nop 0
	global_load_lds_dwordx4 v168, s[46:47]
	ds_read_b128 v[114:117], v179 offset:16384
	ds_read_b128 v[122:125], v179 offset:18432
	ds_read_b128 v[130:133], v180 offset:16384
	ds_read_b128 v[134:137], v180 offset:18432
	ds_read_b128 v[158:161], v179 offset:20480
	ds_read_b128 v[182:185], v179 offset:22528
	ds_read_b128 v[186:189], v180 offset:20480
	ds_read_b128 v[190:193], v180 offset:22528
	s_mov_b32 m0, s53
	s_nop 0
	global_load_lds_dwordx4 v162, s[44:45]
	s_mov_b32 m0, s56
	s_nop 0
	global_load_lds_dwordx4 v166, s[44:45]
	s_add_u32 s46, s46, s22
	s_addc_u32 s47, s47, s23
	s_mov_b32 m0, s57
	s_nop 0
	global_load_lds_dwordx4 v164, s[46:47]
	s_mov_b32 m0, s58
	s_nop 0
	global_load_lds_dwordx4 v168, s[46:47]
	s_waitcnt vmcnt(8)
	s_waitcnt lgkmcnt(0)
	s_barrier
	s_setprio 1
	s_waitcnt lgkmcnt(7)
	v_mfma_f32_16x16x128_f8f6f4 v[86:89], v[82:85], v[114:117], v[14:17] cbsz:4 blgp:4
	s_waitcnt lgkmcnt(5)
	v_mfma_f32_16x16x128_f8f6f4 v[86:89], v[102:105], v[130:133], v[86:89] cbsz:4 blgp:4
	v_mfma_f32_16x16x128_f8f6f4 v[90:93], v[94:97], v[114:117], v[10:13] cbsz:4 blgp:4
	s_nop 0
	v_mfma_f32_16x16x128_f8f6f4 v[90:93], v[110:113], v[130:133], v[90:93] cbsz:4 blgp:4
	v_mfma_f32_16x16x128_f8f6f4 v[98:101], v[82:85], v[122:125], v[14:17] cbsz:4 blgp:4
	s_waitcnt lgkmcnt(4)
	v_mfma_f32_16x16x128_f8f6f4 v[98:101], v[102:105], v[134:137], v[98:101] cbsz:4 blgp:4
	v_mfma_f32_16x16x128_f8f6f4 v[106:109], v[94:97], v[122:125], v[10:13] cbsz:4 blgp:4
	s_nop 0
	v_mfma_f32_16x16x128_f8f6f4 v[106:109], v[110:113], v[134:137], v[106:109] cbsz:4 blgp:4
	s_waitcnt lgkmcnt(3)
	v_mfma_f32_16x16x128_f8f6f4 v[118:121], v[82:85], v[158:161], v[14:17] cbsz:4 blgp:4
	s_waitcnt lgkmcnt(1)
	v_mfma_f32_16x16x128_f8f6f4 v[118:121], v[102:105], v[186:189], v[118:121] cbsz:4 blgp:4
	v_mfma_f32_16x16x128_f8f6f4 v[126:129], v[94:97], v[158:161], v[10:13] cbsz:4 blgp:4
	s_nop 0
	v_mfma_f32_16x16x128_f8f6f4 v[126:129], v[110:113], v[186:189], v[126:129] cbsz:4 blgp:4
	v_mfma_f32_16x16x128_f8f6f4 v[138:141], v[82:85], v[182:185], v[14:17] cbsz:4 blgp:4
	s_waitcnt lgkmcnt(0)
	v_mfma_f32_16x16x128_f8f6f4 v[138:141], v[102:105], v[190:193], v[138:141] cbsz:4 blgp:4
	v_mfma_f32_16x16x128_f8f6f4 v[82:85], v[94:97], v[182:185], v[10:13] cbsz:4 blgp:4
	s_nop 0
	v_mfma_f32_16x16x128_f8f6f4 v[82:85], v[110:113], v[190:193], v[82:85] cbsz:4 blgp:4
	v_mfma_f32_16x16x128_f8f6f4 v[94:97], v[142:145], v[114:117], v[6:9] cbsz:4 blgp:4
	s_nop 0
	v_mfma_f32_16x16x128_f8f6f4 v[94:97], v[150:153], v[130:133], v[94:97] cbsz:4 blgp:4
	v_mfma_f32_16x16x128_f8f6f4 v[102:105], v[146:149], v[114:117], v[2:5] cbsz:4 blgp:4
	s_nop 0
	v_mfma_f32_16x16x128_f8f6f4 v[102:105], v[154:157], v[130:133], v[102:105] cbsz:4 blgp:4
	v_mfma_f32_16x16x128_f8f6f4 v[110:113], v[142:145], v[122:125], v[6:9] cbsz:4 blgp:4
	s_nop 0
	v_mfma_f32_16x16x128_f8f6f4 v[110:113], v[150:153], v[134:137], v[110:113] cbsz:4 blgp:4
	v_mfma_f32_16x16x128_f8f6f4 v[114:117], v[146:149], v[122:125], v[2:5] cbsz:4 blgp:4
	s_nop 0
	v_mfma_f32_16x16x128_f8f6f4 v[114:117], v[154:157], v[134:137], v[114:117] cbsz:4 blgp:4
	v_mfma_f32_16x16x128_f8f6f4 v[122:125], v[142:145], v[158:161], v[6:9] cbsz:4 blgp:4
	s_nop 0
	v_mfma_f32_16x16x128_f8f6f4 v[122:125], v[150:153], v[186:189], v[122:125] cbsz:4 blgp:4
	v_mfma_f32_16x16x128_f8f6f4 v[130:133], v[146:149], v[158:161], v[2:5] cbsz:4 blgp:4
	s_nop 0
	v_mfma_f32_16x16x128_f8f6f4 v[130:133], v[154:157], v[186:189], v[130:133] cbsz:4 blgp:4
	v_mfma_f32_16x16x128_f8f6f4 v[134:137], v[142:145], v[182:185], v[6:9] cbsz:4 blgp:4
	s_nop 0
	v_mfma_f32_16x16x128_f8f6f4 v[134:137], v[150:153], v[190:193], v[134:137] cbsz:4 blgp:4
	v_mfma_f32_16x16x128_f8f6f4 v[142:145], v[146:149], v[182:185], v[2:5] cbsz:4 blgp:4
	s_nop 0
	v_mfma_f32_16x16x128_f8f6f4 v[142:145], v[154:157], v[190:193], v[142:145] cbsz:4 blgp:4
	s_setprio 0
	s_barrier
	ds_read_b128 v[146:149], v169 offset:32768
	ds_read_b128 v[150:153], v169 offset:34816
	ds_read_b128 v[154:157], v178 offset:32768
	ds_read_b128 v[158:161], v178 offset:34816
	ds_read_b128 v[182:185], v179 offset:32768
	ds_read_b128 v[186:189], v179 offset:34816
	ds_read_b128 v[190:193], v180 offset:32768
	ds_read_b128 v[194:197], v180 offset:34816
	ds_read_b128 v[198:201], v179 offset:36864
	ds_read_b128 v[202:205], v179 offset:38912
	ds_read_b128 v[206:209], v180 offset:36864
	ds_read_b128 v[210:213], v180 offset:38912
	s_add_u32 s44, s44, s20
	s_addc_u32 s45, s45, s21
	s_mov_b32 m0, s59
	s_nop 0
	global_load_lds_dwordx4 v162, s[44:45]
	s_mov_b32 m0, s60
	s_nop 0
	global_load_lds_dwordx4 v166, s[44:45]
	s_waitcnt lgkmcnt(8)
	ds_read_b128 v[214:217], v169 offset:49152
	ds_read_b128 v[218:221], v169 offset:51200
	ds_read_b128 v[222:225], v178 offset:49152
	ds_read_b128 v[226:229], v178 offset:51200
	s_waitcnt vmcnt(8)
	s_waitcnt lgkmcnt(0)
	s_barrier
	s_waitcnt lgkmcnt(0)
	s_setprio 1
	s_waitcnt lgkmcnt(7)
	v_mfma_f32_16x16x128_f8f6f4 v[18:21], v[146:149], v[182:185], v[18:21] cbsz:4 blgp:4
	s_waitcnt lgkmcnt(5)
	v_mfma_f32_16x16x128_f8f6f4 v[18:21], v[154:157], v[190:193], v[18:21] cbsz:4 blgp:4
	v_mfma_f32_16x16x128_f8f6f4 v[22:25], v[150:153], v[182:185], v[22:25] cbsz:4 blgp:4
	s_nop 0
	v_mfma_f32_16x16x128_f8f6f4 v[22:25], v[158:161], v[190:193], v[22:25] cbsz:4 blgp:4
	v_mfma_f32_16x16x128_f8f6f4 v[26:29], v[146:149], v[186:189], v[26:29] cbsz:4 blgp:4
	s_waitcnt lgkmcnt(4)
	v_mfma_f32_16x16x128_f8f6f4 v[26:29], v[154:157], v[194:197], v[26:29] cbsz:4 blgp:4
	v_mfma_f32_16x16x128_f8f6f4 v[30:33], v[150:153], v[186:189], v[30:33] cbsz:4 blgp:4
	s_nop 0
	v_mfma_f32_16x16x128_f8f6f4 v[30:33], v[158:161], v[194:197], v[30:33] cbsz:4 blgp:4
	s_waitcnt lgkmcnt(3)
	v_mfma_f32_16x16x128_f8f6f4 v[34:37], v[146:149], v[198:201], v[34:37] cbsz:4 blgp:4
	s_waitcnt lgkmcnt(1)
	v_mfma_f32_16x16x128_f8f6f4 v[34:37], v[154:157], v[206:209], v[34:37] cbsz:4 blgp:4
	v_mfma_f32_16x16x128_f8f6f4 v[38:41], v[150:153], v[198:201], v[38:41] cbsz:4 blgp:4
	s_nop 0
	v_mfma_f32_16x16x128_f8f6f4 v[38:41], v[158:161], v[206:209], v[38:41] cbsz:4 blgp:4
	v_mfma_f32_16x16x128_f8f6f4 v[42:45], v[146:149], v[202:205], v[42:45] cbsz:4 blgp:4
	s_waitcnt lgkmcnt(0)
	v_mfma_f32_16x16x128_f8f6f4 v[42:45], v[154:157], v[210:213], v[42:45] cbsz:4 blgp:4
	v_mfma_f32_16x16x128_f8f6f4 v[46:49], v[150:153], v[202:205], v[46:49] cbsz:4 blgp:4
	s_nop 0
	v_mfma_f32_16x16x128_f8f6f4 v[46:49], v[158:161], v[210:213], v[46:49] cbsz:4 blgp:4
	s_waitcnt lgkmcnt(3)
	v_mfma_f32_16x16x128_f8f6f4 v[50:53], v[214:217], v[182:185], v[50:53] cbsz:4 blgp:4
	s_waitcnt lgkmcnt(1)
	v_mfma_f32_16x16x128_f8f6f4 v[50:53], v[222:225], v[190:193], v[50:53] cbsz:4 blgp:4
	v_mfma_f32_16x16x128_f8f6f4 v[54:57], v[218:221], v[182:185], v[54:57] cbsz:4 blgp:4
	s_waitcnt lgkmcnt(0)
	v_mfma_f32_16x16x128_f8f6f4 v[54:57], v[226:229], v[190:193], v[54:57] cbsz:4 blgp:4
	v_mfma_f32_16x16x128_f8f6f4 v[58:61], v[214:217], v[186:189], v[58:61] cbsz:4 blgp:4
	s_nop 0
	v_mfma_f32_16x16x128_f8f6f4 v[58:61], v[222:225], v[194:197], v[58:61] cbsz:4 blgp:4
	v_mfma_f32_16x16x128_f8f6f4 v[62:65], v[218:221], v[186:189], v[62:65] cbsz:4 blgp:4
	s_nop 0
	v_mfma_f32_16x16x128_f8f6f4 v[62:65], v[226:229], v[194:197], v[62:65] cbsz:4 blgp:4
	v_mfma_f32_16x16x128_f8f6f4 v[66:69], v[214:217], v[198:201], v[66:69] cbsz:4 blgp:4
	s_nop 0
	v_mfma_f32_16x16x128_f8f6f4 v[66:69], v[222:225], v[206:209], v[66:69] cbsz:4 blgp:4
	v_mfma_f32_16x16x128_f8f6f4 v[70:73], v[218:221], v[198:201], v[70:73] cbsz:4 blgp:4
	s_nop 0
	v_mfma_f32_16x16x128_f8f6f4 v[70:73], v[226:229], v[206:209], v[70:73] cbsz:4 blgp:4
	v_mfma_f32_16x16x128_f8f6f4 v[74:77], v[214:217], v[202:205], v[74:77] cbsz:4 blgp:4
	s_nop 0
	v_mfma_f32_16x16x128_f8f6f4 v[74:77], v[222:225], v[210:213], v[74:77] cbsz:4 blgp:4
	v_mfma_f32_16x16x128_f8f6f4 v[78:81], v[218:221], v[202:205], v[78:81] cbsz:4 blgp:4
	s_nop 0
	v_mfma_f32_16x16x128_f8f6f4 v[78:81], v[226:229], v[210:213], v[78:81] cbsz:4 blgp:4
	s_setprio 0
	s_barrier
	s_mov_b32 m0, s62
	s_nop 0
	global_load_lds_dwordx4 v164, s[40:41]
	s_mov_b32 m0, s63
	s_nop 0
	global_load_lds_dwordx4 v168, s[40:41]
	ds_read_b128 v[182:185], v179 offset:49152
	ds_read_b128 v[186:189], v179 offset:51200
	ds_read_b128 v[190:193], v180 offset:49152
	ds_read_b128 v[194:197], v180 offset:51200
	ds_read_b128 v[198:201], v179 offset:53248
	ds_read_b128 v[202:205], v179 offset:55296
	ds_read_b128 v[206:209], v180 offset:53248
	ds_read_b128 v[210:213], v180 offset:55296
	s_mov_b32 m0, s64
	s_nop 0
	global_load_lds_dwordx4 v162, s[42:43]
	s_mov_b32 m0, s65
	s_nop 0
	global_load_lds_dwordx4 v166, s[42:43]
	s_add_u32 s40, s40, s22
	s_addc_u32 s41, s41, s23
	s_mov_b32 m0, s66
	s_nop 0
	global_load_lds_dwordx4 v164, s[40:41]
	s_mov_b32 m0, s67
	s_nop 0
	global_load_lds_dwordx4 v168, s[40:41]
	s_waitcnt vmcnt(8)
	s_waitcnt lgkmcnt(0)
	s_barrier
	s_setprio 1
	s_waitcnt lgkmcnt(7)
	v_mfma_f32_16x16x128_f8f6f4 v[86:89], v[146:149], v[182:185], v[86:89] cbsz:4 blgp:4
	s_waitcnt lgkmcnt(5)
	v_mfma_f32_16x16x128_f8f6f4 v[86:89], v[154:157], v[190:193], v[86:89] cbsz:4 blgp:4
	v_mfma_f32_16x16x128_f8f6f4 v[90:93], v[150:153], v[182:185], v[90:93] cbsz:4 blgp:4
	s_nop 0
	v_mfma_f32_16x16x128_f8f6f4 v[90:93], v[158:161], v[190:193], v[90:93] cbsz:4 blgp:4
	v_mfma_f32_16x16x128_f8f6f4 v[98:101], v[146:149], v[186:189], v[98:101] cbsz:4 blgp:4
	s_waitcnt lgkmcnt(4)
	v_mfma_f32_16x16x128_f8f6f4 v[98:101], v[154:157], v[194:197], v[98:101] cbsz:4 blgp:4
	v_mfma_f32_16x16x128_f8f6f4 v[106:109], v[150:153], v[186:189], v[106:109] cbsz:4 blgp:4
	s_nop 0
	v_mfma_f32_16x16x128_f8f6f4 v[106:109], v[158:161], v[194:197], v[106:109] cbsz:4 blgp:4
	s_waitcnt lgkmcnt(3)
	v_mfma_f32_16x16x128_f8f6f4 v[118:121], v[146:149], v[198:201], v[118:121] cbsz:4 blgp:4
	s_waitcnt lgkmcnt(1)
	v_mfma_f32_16x16x128_f8f6f4 v[118:121], v[154:157], v[206:209], v[118:121] cbsz:4 blgp:4
	v_mfma_f32_16x16x128_f8f6f4 v[126:129], v[150:153], v[198:201], v[126:129] cbsz:4 blgp:4
	s_nop 0
	v_mfma_f32_16x16x128_f8f6f4 v[126:129], v[158:161], v[206:209], v[126:129] cbsz:4 blgp:4
	v_mfma_f32_16x16x128_f8f6f4 v[138:141], v[146:149], v[202:205], v[138:141] cbsz:4 blgp:4
	s_waitcnt lgkmcnt(0)
	v_mfma_f32_16x16x128_f8f6f4 v[138:141], v[154:157], v[210:213], v[138:141] cbsz:4 blgp:4
	v_mfma_f32_16x16x128_f8f6f4 v[82:85], v[150:153], v[202:205], v[82:85] cbsz:4 blgp:4
	s_nop 0
	v_mfma_f32_16x16x128_f8f6f4 v[82:85], v[158:161], v[210:213], v[82:85] cbsz:4 blgp:4
	v_mfma_f32_16x16x128_f8f6f4 v[94:97], v[214:217], v[182:185], v[94:97] cbsz:4 blgp:4
	s_nop 0
	v_mfma_f32_16x16x128_f8f6f4 v[94:97], v[222:225], v[190:193], v[94:97] cbsz:4 blgp:4
	v_mfma_f32_16x16x128_f8f6f4 v[102:105], v[218:221], v[182:185], v[102:105] cbsz:4 blgp:4
	s_nop 0
	v_mfma_f32_16x16x128_f8f6f4 v[102:105], v[226:229], v[190:193], v[102:105] cbsz:4 blgp:4
	v_mfma_f32_16x16x128_f8f6f4 v[110:113], v[214:217], v[186:189], v[110:113] cbsz:4 blgp:4
	s_nop 0
	v_mfma_f32_16x16x128_f8f6f4 v[110:113], v[222:225], v[194:197], v[110:113] cbsz:4 blgp:4
	v_mfma_f32_16x16x128_f8f6f4 v[114:117], v[218:221], v[186:189], v[114:117] cbsz:4 blgp:4
	s_nop 0
	v_mfma_f32_16x16x128_f8f6f4 v[114:117], v[226:229], v[194:197], v[114:117] cbsz:4 blgp:4
	v_mfma_f32_16x16x128_f8f6f4 v[122:125], v[214:217], v[198:201], v[122:125] cbsz:4 blgp:4
	s_nop 0
	v_mfma_f32_16x16x128_f8f6f4 v[122:125], v[222:225], v[206:209], v[122:125] cbsz:4 blgp:4
	v_mfma_f32_16x16x128_f8f6f4 v[130:133], v[218:221], v[198:201], v[130:133] cbsz:4 blgp:4
	s_nop 0
	v_mfma_f32_16x16x128_f8f6f4 v[130:133], v[226:229], v[206:209], v[130:133] cbsz:4 blgp:4
	v_mfma_f32_16x16x128_f8f6f4 v[134:137], v[214:217], v[202:205], v[134:137] cbsz:4 blgp:4
	s_nop 0
	v_mfma_f32_16x16x128_f8f6f4 v[134:137], v[222:225], v[210:213], v[134:137] cbsz:4 blgp:4
	v_mfma_f32_16x16x128_f8f6f4 v[142:145], v[218:221], v[202:205], v[142:145] cbsz:4 blgp:4
	s_nop 0
	v_mfma_f32_16x16x128_f8f6f4 v[142:145], v[226:229], v[210:213], v[142:145] cbsz:4 blgp:4
	s_setprio 0
	s_andn2_b64 vcc, exec, s[28:29]
	s_barrier
	s_cbranch_vccnz .LBB6_20
	s_ashr_i32 s39, s38, 31
	s_lshl_b64 s[38:39], s[38:39], 10
	s_add_u32 s38, s14, s38
	s_addc_u32 s39, s15, s39
	s_add_u32 s31, s36, 0x200
	s_addc_u32 s46, s37, 0
	s_add_u32 s47, s34, 0x200
	s_addc_u32 s81, s35, 0
	s_add_u32 s34, s82, 0x180
	s_addc_u32 s35, s83, 0
	s_mov_b32 s82, 4
	s_cmp_eq_u32 s61, s82
	s_cselect_b64 s[36:37], -1, 0
	s_cmp_lg_u32 s61, s82
	s_cbranch_scc1 .LBB6_18

.LBB6_18:
	ds_read_b128 v[146:149], v169
	ds_read_b128 v[150:153], v169 offset:2048
	ds_read_b128 v[154:157], v178
	ds_read_b128 v[158:161], v178 offset:2048
	s_and_b64 s[36:37], s[36:37], exec
	s_cselect_b32 s42, s4, s31
	s_cselect_b32 s43, s5, s46
	s_cselect_b32 s45, s7, s81
	s_cselect_b32 s44, s6, s47
	s_add_u32 s40, s42, 0x80
	s_addc_u32 s41, s43, 0
	s_add_u32 s36, s44, 0x80
	s_addc_u32 s37, s45, 0
	ds_read_b128 v[182:185], v179
	ds_read_b128 v[186:189], v179 offset:2048
	ds_read_b128 v[190:193], v180
	ds_read_b128 v[194:197], v180 offset:2048
	ds_read_b128 v[198:201], v179 offset:4096
	ds_read_b128 v[202:205], v179 offset:6144
	ds_read_b128 v[206:209], v180 offset:4096
	ds_read_b128 v[210:213], v180 offset:6144
	s_mov_b32 m0, s68
	s_nop 0
	global_load_lds_dwordx4 v162, s[34:35]
	s_mov_b32 m0, s69
	s_nop 0
	global_load_lds_dwordx4 v166, s[34:35]
	s_waitcnt lgkmcnt(8)
	ds_read_b128 v[214:217], v169 offset:16384
	ds_read_b128 v[218:221], v169 offset:18432
	ds_read_b128 v[222:225], v178 offset:16384
	ds_read_b128 v[226:229], v178 offset:18432
	s_waitcnt vmcnt(8)
	s_waitcnt lgkmcnt(0)
	s_barrier
	s_waitcnt lgkmcnt(0)
	s_setprio 1
	s_waitcnt lgkmcnt(7)
	v_mfma_f32_16x16x128_f8f6f4 v[18:21], v[146:149], v[182:185], v[18:21] cbsz:4 blgp:4
	s_waitcnt lgkmcnt(5)
	v_mfma_f32_16x16x128_f8f6f4 v[18:21], v[154:157], v[190:193], v[18:21] cbsz:4 blgp:4
	v_mfma_f32_16x16x128_f8f6f4 v[22:25], v[150:153], v[182:185], v[22:25] cbsz:4 blgp:4
	s_nop 0
	v_mfma_f32_16x16x128_f8f6f4 v[22:25], v[158:161], v[190:193], v[22:25] cbsz:4 blgp:4
	v_mfma_f32_16x16x128_f8f6f4 v[26:29], v[146:149], v[186:189], v[26:29] cbsz:4 blgp:4
	s_waitcnt lgkmcnt(4)
	v_mfma_f32_16x16x128_f8f6f4 v[26:29], v[154:157], v[194:197], v[26:29] cbsz:4 blgp:4
	v_mfma_f32_16x16x128_f8f6f4 v[30:33], v[150:153], v[186:189], v[30:33] cbsz:4 blgp:4
	s_nop 0
	v_mfma_f32_16x16x128_f8f6f4 v[30:33], v[158:161], v[194:197], v[30:33] cbsz:4 blgp:4
	s_waitcnt lgkmcnt(3)
	v_mfma_f32_16x16x128_f8f6f4 v[34:37], v[146:149], v[198:201], v[34:37] cbsz:4 blgp:4
	s_waitcnt lgkmcnt(1)
	v_mfma_f32_16x16x128_f8f6f4 v[34:37], v[154:157], v[206:209], v[34:37] cbsz:4 blgp:4
	v_mfma_f32_16x16x128_f8f6f4 v[38:41], v[150:153], v[198:201], v[38:41] cbsz:4 blgp:4
	s_nop 0
	v_mfma_f32_16x16x128_f8f6f4 v[38:41], v[158:161], v[206:209], v[38:41] cbsz:4 blgp:4
	v_mfma_f32_16x16x128_f8f6f4 v[42:45], v[146:149], v[202:205], v[42:45] cbsz:4 blgp:4
	s_waitcnt lgkmcnt(0)
	v_mfma_f32_16x16x128_f8f6f4 v[42:45], v[154:157], v[210:213], v[42:45] cbsz:4 blgp:4
	v_mfma_f32_16x16x128_f8f6f4 v[46:49], v[150:153], v[202:205], v[46:49] cbsz:4 blgp:4
	s_nop 0
	v_mfma_f32_16x16x128_f8f6f4 v[46:49], v[158:161], v[210:213], v[46:49] cbsz:4 blgp:4
	s_waitcnt lgkmcnt(3)
	v_mfma_f32_16x16x128_f8f6f4 v[50:53], v[214:217], v[182:185], v[50:53] cbsz:4 blgp:4
	s_waitcnt lgkmcnt(1)
	v_mfma_f32_16x16x128_f8f6f4 v[50:53], v[222:225], v[190:193], v[50:53] cbsz:4 blgp:4
	v_mfma_f32_16x16x128_f8f6f4 v[54:57], v[218:221], v[182:185], v[54:57] cbsz:4 blgp:4
	s_waitcnt lgkmcnt(0)
	v_mfma_f32_16x16x128_f8f6f4 v[54:57], v[226:229], v[190:193], v[54:57] cbsz:4 blgp:4
	v_mfma_f32_16x16x128_f8f6f4 v[58:61], v[214:217], v[186:189], v[58:61] cbsz:4 blgp:4
	s_nop 0
	v_mfma_f32_16x16x128_f8f6f4 v[58:61], v[222:225], v[194:197], v[58:61] cbsz:4 blgp:4
	v_mfma_f32_16x16x128_f8f6f4 v[62:65], v[218:221], v[186:189], v[62:65] cbsz:4 blgp:4
	s_nop 0
	v_mfma_f32_16x16x128_f8f6f4 v[62:65], v[226:229], v[194:197], v[62:65] cbsz:4 blgp:4
	v_mfma_f32_16x16x128_f8f6f4 v[66:69], v[214:217], v[198:201], v[66:69] cbsz:4 blgp:4
	s_nop 0
	v_mfma_f32_16x16x128_f8f6f4 v[66:69], v[222:225], v[206:209], v[66:69] cbsz:4 blgp:4
	v_mfma_f32_16x16x128_f8f6f4 v[70:73], v[218:221], v[198:201], v[70:73] cbsz:4 blgp:4
	s_nop 0
	v_mfma_f32_16x16x128_f8f6f4 v[70:73], v[226:229], v[206:209], v[70:73] cbsz:4 blgp:4
	v_mfma_f32_16x16x128_f8f6f4 v[74:77], v[214:217], v[202:205], v[74:77] cbsz:4 blgp:4
	s_nop 0
	v_mfma_f32_16x16x128_f8f6f4 v[74:77], v[222:225], v[210:213], v[74:77] cbsz:4 blgp:4
	v_mfma_f32_16x16x128_f8f6f4 v[78:81], v[218:221], v[202:205], v[78:81] cbsz:4 blgp:4
	s_nop 0
	v_mfma_f32_16x16x128_f8f6f4 v[78:81], v[226:229], v[210:213], v[78:81] cbsz:4 blgp:4
	s_setprio 0
	s_barrier
	s_mov_b32 m0, s54
	s_nop 0
	global_load_lds_dwordx4 v164, s[44:45]
	s_mov_b32 m0, s55
	s_nop 0
	global_load_lds_dwordx4 v168, s[44:45]
	ds_read_b128 v[182:185], v179 offset:16384
	ds_read_b128 v[186:189], v179 offset:18432
	ds_read_b128 v[190:193], v180 offset:16384
	ds_read_b128 v[194:197], v180 offset:18432
	ds_read_b128 v[198:201], v179 offset:20480
	ds_read_b128 v[202:205], v179 offset:22528
	ds_read_b128 v[206:209], v180 offset:20480
	ds_read_b128 v[210:213], v180 offset:22528
	s_mov_b32 m0, s53
	s_nop 0
	global_load_lds_dwordx4 v162, s[42:43]
	s_mov_b32 m0, s56
	s_nop 0
	global_load_lds_dwordx4 v166, s[42:43]
	s_add_u32 s44, s44, s22
	s_addc_u32 s45, s45, s23
	s_mov_b32 m0, s57
	s_nop 0
	global_load_lds_dwordx4 v164, s[44:45]
	s_mov_b32 m0, s58
	s_nop 0
	global_load_lds_dwordx4 v168, s[44:45]
	s_waitcnt vmcnt(8)
	s_waitcnt lgkmcnt(0)
	s_barrier
	s_setprio 1
	s_waitcnt lgkmcnt(7)
	v_mfma_f32_16x16x128_f8f6f4 v[86:89], v[146:149], v[182:185], v[86:89] cbsz:4 blgp:4
	s_waitcnt lgkmcnt(5)
	v_mfma_f32_16x16x128_f8f6f4 v[86:89], v[154:157], v[190:193], v[86:89] cbsz:4 blgp:4
	v_mfma_f32_16x16x128_f8f6f4 v[90:93], v[150:153], v[182:185], v[90:93] cbsz:4 blgp:4
	s_nop 0
	v_mfma_f32_16x16x128_f8f6f4 v[90:93], v[158:161], v[190:193], v[90:93] cbsz:4 blgp:4
	v_mfma_f32_16x16x128_f8f6f4 v[98:101], v[146:149], v[186:189], v[98:101] cbsz:4 blgp:4
	s_waitcnt lgkmcnt(4)
	v_mfma_f32_16x16x128_f8f6f4 v[98:101], v[154:157], v[194:197], v[98:101] cbsz:4 blgp:4
	v_mfma_f32_16x16x128_f8f6f4 v[106:109], v[150:153], v[186:189], v[106:109] cbsz:4 blgp:4
	s_nop 0
	v_mfma_f32_16x16x128_f8f6f4 v[106:109], v[158:161], v[194:197], v[106:109] cbsz:4 blgp:4
	s_waitcnt lgkmcnt(3)
	v_mfma_f32_16x16x128_f8f6f4 v[118:121], v[146:149], v[198:201], v[118:121] cbsz:4 blgp:4
	s_waitcnt lgkmcnt(1)
	v_mfma_f32_16x16x128_f8f6f4 v[118:121], v[154:157], v[206:209], v[118:121] cbsz:4 blgp:4
	v_mfma_f32_16x16x128_f8f6f4 v[126:129], v[150:153], v[198:201], v[126:129] cbsz:4 blgp:4
	s_nop 0
	v_mfma_f32_16x16x128_f8f6f4 v[126:129], v[158:161], v[206:209], v[126:129] cbsz:4 blgp:4
	v_mfma_f32_16x16x128_f8f6f4 v[138:141], v[146:149], v[202:205], v[138:141] cbsz:4 blgp:4
	s_waitcnt lgkmcnt(0)
	v_mfma_f32_16x16x128_f8f6f4 v[138:141], v[154:157], v[210:213], v[138:141] cbsz:4 blgp:4
	v_mfma_f32_16x16x128_f8f6f4 v[82:85], v[150:153], v[202:205], v[82:85] cbsz:4 blgp:4
	s_nop 0
	v_mfma_f32_16x16x128_f8f6f4 v[82:85], v[158:161], v[210:213], v[82:85] cbsz:4 blgp:4
	v_mfma_f32_16x16x128_f8f6f4 v[94:97], v[214:217], v[182:185], v[94:97] cbsz:4 blgp:4
	s_nop 0
	v_mfma_f32_16x16x128_f8f6f4 v[94:97], v[222:225], v[190:193], v[94:97] cbsz:4 blgp:4
	v_mfma_f32_16x16x128_f8f6f4 v[102:105], v[218:221], v[182:185], v[102:105] cbsz:4 blgp:4
	s_nop 0
	v_mfma_f32_16x16x128_f8f6f4 v[102:105], v[226:229], v[190:193], v[102:105] cbsz:4 blgp:4
	v_mfma_f32_16x16x128_f8f6f4 v[110:113], v[214:217], v[186:189], v[110:113] cbsz:4 blgp:4
	s_nop 0
	v_mfma_f32_16x16x128_f8f6f4 v[110:113], v[222:225], v[194:197], v[110:113] cbsz:4 blgp:4
	v_mfma_f32_16x16x128_f8f6f4 v[114:117], v[218:221], v[186:189], v[114:117] cbsz:4 blgp:4
	s_nop 0
	v_mfma_f32_16x16x128_f8f6f4 v[114:117], v[226:229], v[194:197], v[114:117] cbsz:4 blgp:4
	v_mfma_f32_16x16x128_f8f6f4 v[122:125], v[214:217], v[198:201], v[122:125] cbsz:4 blgp:4
	s_nop 0
	v_mfma_f32_16x16x128_f8f6f4 v[122:125], v[222:225], v[206:209], v[122:125] cbsz:4 blgp:4
	v_mfma_f32_16x16x128_f8f6f4 v[130:133], v[218:221], v[198:201], v[130:133] cbsz:4 blgp:4
	s_nop 0
	v_mfma_f32_16x16x128_f8f6f4 v[130:133], v[226:229], v[206:209], v[130:133] cbsz:4 blgp:4
	v_mfma_f32_16x16x128_f8f6f4 v[134:137], v[214:217], v[202:205], v[134:137] cbsz:4 blgp:4
	s_nop 0
	v_mfma_f32_16x16x128_f8f6f4 v[134:137], v[222:225], v[210:213], v[134:137] cbsz:4 blgp:4
	v_mfma_f32_16x16x128_f8f6f4 v[142:145], v[218:221], v[202:205], v[142:145] cbsz:4 blgp:4
	s_nop 0
	v_mfma_f32_16x16x128_f8f6f4 v[142:145], v[226:229], v[210:213], v[142:145] cbsz:4 blgp:4
	s_setprio 0
	s_barrier
	ds_read_b128 v[146:149], v169 offset:32768
	ds_read_b128 v[150:153], v169 offset:34816
	ds_read_b128 v[154:157], v178 offset:32768
	ds_read_b128 v[158:161], v178 offset:34816
	ds_read_b128 v[182:185], v179 offset:32768
	ds_read_b128 v[186:189], v179 offset:34816
	ds_read_b128 v[190:193], v180 offset:32768
	ds_read_b128 v[194:197], v180 offset:34816
	ds_read_b128 v[198:201], v179 offset:36864
	ds_read_b128 v[202:205], v179 offset:38912
	ds_read_b128 v[206:209], v180 offset:36864
	ds_read_b128 v[210:213], v180 offset:38912
	s_add_u32 s42, s42, s20
	s_addc_u32 s43, s43, s21
	s_mov_b32 m0, s59
	s_nop 0
	global_load_lds_dwordx4 v162, s[42:43]
	s_mov_b32 m0, s60
	s_nop 0
	global_load_lds_dwordx4 v166, s[42:43]
	s_waitcnt lgkmcnt(8)
	ds_read_b128 v[214:217], v169 offset:49152
	ds_read_b128 v[218:221], v169 offset:51200
	ds_read_b128 v[222:225], v178 offset:49152
	ds_read_b128 v[226:229], v178 offset:51200
	s_waitcnt vmcnt(8)
	s_waitcnt lgkmcnt(0)
	s_barrier
	s_waitcnt lgkmcnt(0)
	s_setprio 1
	s_waitcnt lgkmcnt(7)
	v_mfma_f32_16x16x128_f8f6f4 v[18:21], v[146:149], v[182:185], v[18:21] cbsz:4 blgp:4
	s_waitcnt lgkmcnt(5)
	v_mfma_f32_16x16x128_f8f6f4 v[18:21], v[154:157], v[190:193], v[18:21] cbsz:4 blgp:4
	v_mfma_f32_16x16x128_f8f6f4 v[22:25], v[150:153], v[182:185], v[22:25] cbsz:4 blgp:4
	s_nop 0
	v_mfma_f32_16x16x128_f8f6f4 v[22:25], v[158:161], v[190:193], v[22:25] cbsz:4 blgp:4
	v_mfma_f32_16x16x128_f8f6f4 v[26:29], v[146:149], v[186:189], v[26:29] cbsz:4 blgp:4
	s_waitcnt lgkmcnt(4)
	v_mfma_f32_16x16x128_f8f6f4 v[26:29], v[154:157], v[194:197], v[26:29] cbsz:4 blgp:4
	v_mfma_f32_16x16x128_f8f6f4 v[30:33], v[150:153], v[186:189], v[30:33] cbsz:4 blgp:4
	s_nop 0
	v_mfma_f32_16x16x128_f8f6f4 v[30:33], v[158:161], v[194:197], v[30:33] cbsz:4 blgp:4
	s_waitcnt lgkmcnt(3)
	v_mfma_f32_16x16x128_f8f6f4 v[34:37], v[146:149], v[198:201], v[34:37] cbsz:4 blgp:4
	s_waitcnt lgkmcnt(1)
	v_mfma_f32_16x16x128_f8f6f4 v[34:37], v[154:157], v[206:209], v[34:37] cbsz:4 blgp:4
	v_mfma_f32_16x16x128_f8f6f4 v[38:41], v[150:153], v[198:201], v[38:41] cbsz:4 blgp:4
	s_nop 0
	v_mfma_f32_16x16x128_f8f6f4 v[38:41], v[158:161], v[206:209], v[38:41] cbsz:4 blgp:4
	v_mfma_f32_16x16x128_f8f6f4 v[42:45], v[146:149], v[202:205], v[42:45] cbsz:4 blgp:4
	s_waitcnt lgkmcnt(0)
	v_mfma_f32_16x16x128_f8f6f4 v[42:45], v[154:157], v[210:213], v[42:45] cbsz:4 blgp:4
	v_mfma_f32_16x16x128_f8f6f4 v[46:49], v[150:153], v[202:205], v[46:49] cbsz:4 blgp:4
	s_nop 0
	v_mfma_f32_16x16x128_f8f6f4 v[46:49], v[158:161], v[210:213], v[46:49] cbsz:4 blgp:4
	s_waitcnt lgkmcnt(3)
	v_mfma_f32_16x16x128_f8f6f4 v[50:53], v[214:217], v[182:185], v[50:53] cbsz:4 blgp:4
	s_waitcnt lgkmcnt(1)
	v_mfma_f32_16x16x128_f8f6f4 v[50:53], v[222:225], v[190:193], v[50:53] cbsz:4 blgp:4
	v_mfma_f32_16x16x128_f8f6f4 v[54:57], v[218:221], v[182:185], v[54:57] cbsz:4 blgp:4
	s_waitcnt lgkmcnt(0)
	v_mfma_f32_16x16x128_f8f6f4 v[54:57], v[226:229], v[190:193], v[54:57] cbsz:4 blgp:4
	v_mfma_f32_16x16x128_f8f6f4 v[58:61], v[214:217], v[186:189], v[58:61] cbsz:4 blgp:4
	s_nop 0
	v_mfma_f32_16x16x128_f8f6f4 v[58:61], v[222:225], v[194:197], v[58:61] cbsz:4 blgp:4
	v_mfma_f32_16x16x128_f8f6f4 v[62:65], v[218:221], v[186:189], v[62:65] cbsz:4 blgp:4
	s_nop 0
	v_mfma_f32_16x16x128_f8f6f4 v[62:65], v[226:229], v[194:197], v[62:65] cbsz:4 blgp:4
	v_mfma_f32_16x16x128_f8f6f4 v[66:69], v[214:217], v[198:201], v[66:69] cbsz:4 blgp:4
	s_nop 0
	v_mfma_f32_16x16x128_f8f6f4 v[66:69], v[222:225], v[206:209], v[66:69] cbsz:4 blgp:4
	v_mfma_f32_16x16x128_f8f6f4 v[70:73], v[218:221], v[198:201], v[70:73] cbsz:4 blgp:4
	s_nop 0
	v_mfma_f32_16x16x128_f8f6f4 v[70:73], v[226:229], v[206:209], v[70:73] cbsz:4 blgp:4
	v_mfma_f32_16x16x128_f8f6f4 v[74:77], v[214:217], v[202:205], v[74:77] cbsz:4 blgp:4
	s_nop 0
	v_mfma_f32_16x16x128_f8f6f4 v[74:77], v[222:225], v[210:213], v[74:77] cbsz:4 blgp:4
	v_mfma_f32_16x16x128_f8f6f4 v[78:81], v[218:221], v[202:205], v[78:81] cbsz:4 blgp:4
	s_nop 0
	v_mfma_f32_16x16x128_f8f6f4 v[78:81], v[226:229], v[210:213], v[78:81] cbsz:4 blgp:4
	s_setprio 0
	s_barrier
	s_mov_b32 m0, s62
	s_nop 0
	global_load_lds_dwordx4 v164, s[36:37]
	s_mov_b32 m0, s63
	s_nop 0
	global_load_lds_dwordx4 v168, s[36:37]
	ds_read_b128 v[182:185], v179 offset:49152
	ds_read_b128 v[186:189], v179 offset:51200
	ds_read_b128 v[190:193], v180 offset:49152
	ds_read_b128 v[194:197], v180 offset:51200
	ds_read_b128 v[198:201], v179 offset:53248
	ds_read_b128 v[202:205], v179 offset:55296
	ds_read_b128 v[206:209], v180 offset:53248
	ds_read_b128 v[210:213], v180 offset:55296
	s_mov_b32 m0, s64
	s_nop 0
	global_load_lds_dwordx4 v162, s[40:41]
	s_mov_b32 m0, s65
	s_nop 0
	global_load_lds_dwordx4 v166, s[40:41]
	s_add_u32 s36, s36, s22
	s_addc_u32 s37, s37, s23
	s_mov_b32 m0, s66
	s_nop 0
	global_load_lds_dwordx4 v164, s[36:37]
	s_mov_b32 m0, s67
	s_nop 0
	global_load_lds_dwordx4 v168, s[36:37]
	s_waitcnt vmcnt(8)
	s_waitcnt lgkmcnt(0)
	s_barrier
	s_setprio 1
	s_waitcnt lgkmcnt(7)
	v_mfma_f32_16x16x128_f8f6f4 v[86:89], v[146:149], v[182:185], v[86:89] cbsz:4 blgp:4
	s_waitcnt lgkmcnt(5)
	v_mfma_f32_16x16x128_f8f6f4 v[86:89], v[154:157], v[190:193], v[86:89] cbsz:4 blgp:4
	v_mfma_f32_16x16x128_f8f6f4 v[90:93], v[150:153], v[182:185], v[90:93] cbsz:4 blgp:4
	s_nop 0
	v_mfma_f32_16x16x128_f8f6f4 v[90:93], v[158:161], v[190:193], v[90:93] cbsz:4 blgp:4
	v_mfma_f32_16x16x128_f8f6f4 v[98:101], v[146:149], v[186:189], v[98:101] cbsz:4 blgp:4
	s_waitcnt lgkmcnt(4)
	v_mfma_f32_16x16x128_f8f6f4 v[98:101], v[154:157], v[194:197], v[98:101] cbsz:4 blgp:4
	v_mfma_f32_16x16x128_f8f6f4 v[106:109], v[150:153], v[186:189], v[106:109] cbsz:4 blgp:4
	s_nop 0
	v_mfma_f32_16x16x128_f8f6f4 v[106:109], v[158:161], v[194:197], v[106:109] cbsz:4 blgp:4
	s_waitcnt lgkmcnt(3)
	v_mfma_f32_16x16x128_f8f6f4 v[118:121], v[146:149], v[198:201], v[118:121] cbsz:4 blgp:4
	s_waitcnt lgkmcnt(1)
	v_mfma_f32_16x16x128_f8f6f4 v[118:121], v[154:157], v[206:209], v[118:121] cbsz:4 blgp:4
	v_mfma_f32_16x16x128_f8f6f4 v[126:129], v[150:153], v[198:201], v[126:129] cbsz:4 blgp:4
	s_nop 0
	v_mfma_f32_16x16x128_f8f6f4 v[126:129], v[158:161], v[206:209], v[126:129] cbsz:4 blgp:4
	v_mfma_f32_16x16x128_f8f6f4 v[138:141], v[146:149], v[202:205], v[138:141] cbsz:4 blgp:4
	s_waitcnt lgkmcnt(0)
	v_mfma_f32_16x16x128_f8f6f4 v[138:141], v[154:157], v[210:213], v[138:141] cbsz:4 blgp:4
	v_mfma_f32_16x16x128_f8f6f4 v[82:85], v[150:153], v[202:205], v[82:85] cbsz:4 blgp:4
	s_nop 0
	v_mfma_f32_16x16x128_f8f6f4 v[82:85], v[158:161], v[210:213], v[82:85] cbsz:4 blgp:4
	v_mfma_f32_16x16x128_f8f6f4 v[94:97], v[214:217], v[182:185], v[94:97] cbsz:4 blgp:4
	s_nop 0
	v_mfma_f32_16x16x128_f8f6f4 v[94:97], v[222:225], v[190:193], v[94:97] cbsz:4 blgp:4
	v_mfma_f32_16x16x128_f8f6f4 v[102:105], v[218:221], v[182:185], v[102:105] cbsz:4 blgp:4
	s_nop 0
	v_mfma_f32_16x16x128_f8f6f4 v[102:105], v[226:229], v[190:193], v[102:105] cbsz:4 blgp:4
	v_mfma_f32_16x16x128_f8f6f4 v[110:113], v[214:217], v[186:189], v[110:113] cbsz:4 blgp:4
	s_nop 0
	v_mfma_f32_16x16x128_f8f6f4 v[110:113], v[222:225], v[194:197], v[110:113] cbsz:4 blgp:4
	v_mfma_f32_16x16x128_f8f6f4 v[114:117], v[218:221], v[186:189], v[114:117] cbsz:4 blgp:4
	s_nop 0
	v_mfma_f32_16x16x128_f8f6f4 v[114:117], v[226:229], v[194:197], v[114:117] cbsz:4 blgp:4
	v_mfma_f32_16x16x128_f8f6f4 v[122:125], v[214:217], v[198:201], v[122:125] cbsz:4 blgp:4
	s_nop 0
	v_mfma_f32_16x16x128_f8f6f4 v[122:125], v[222:225], v[206:209], v[122:125] cbsz:4 blgp:4
	v_mfma_f32_16x16x128_f8f6f4 v[130:133], v[218:221], v[198:201], v[130:133] cbsz:4 blgp:4
	s_nop 0
	v_mfma_f32_16x16x128_f8f6f4 v[130:133], v[226:229], v[206:209], v[130:133] cbsz:4 blgp:4
	v_mfma_f32_16x16x128_f8f6f4 v[134:137], v[214:217], v[202:205], v[134:137] cbsz:4 blgp:4
	s_nop 0
	v_mfma_f32_16x16x128_f8f6f4 v[134:137], v[222:225], v[210:213], v[134:137] cbsz:4 blgp:4
	v_mfma_f32_16x16x128_f8f6f4 v[142:145], v[218:221], v[202:205], v[142:145] cbsz:4 blgp:4
	s_nop 0
	v_mfma_f32_16x16x128_f8f6f4 v[142:145], v[226:229], v[210:213], v[142:145] cbsz:4 blgp:4
	s_setprio 0
	s_add_i32 s36, s82, 2
	s_add_u32 s31, s31, 0x100
	s_addc_u32 s46, s46, 0
	s_add_u32 s47, s47, 0x100
	s_addc_u32 s81, s81, 0
	s_add_u32 s34, s34, 0x100
	s_addc_u32 s35, s35, 0
	s_cmp_ge_i32 s82, s61
	s_barrier
	s_cbranch_scc1 .LBB6_20
	s_mov_b32 s82, s36
	s_cmp_eq_u32 s61, s82
	s_cselect_b64 s[36:37], -1, 0
	s_cmp_lg_u32 s61, s82
	s_cbranch_scc0 .LBB6_17
	s_branch .LBB6_18
